# best6: holdA4 chains + static prio + LDS-DMA addresses formed with scalar adds (saddr form) in all five steady loops
# speedup vs baseline: 1.0235x; 1.0038x over previous
.LBB0_130:
	ds_read_b128 v[144:147], v140
	ds_read_b128 v[148:151], v140 offset:1024
	ds_read_b128 v[152:155], v140 offset:2048
	ds_read_b128 v[156:159], v140 offset:3072
	ds_read_b128 v[164:167], v141
	ds_read_b128 v[168:171], v141 offset:1024
	ds_read_b128 v[172:175], v141 offset:2048
	ds_read_b128 v[176:179], v141 offset:3072
	s_add_u32 s31, s10, 0xfff7c080
	s_addc_u32 s53, s11, -1
	s_cmp_eq_u32 s30, 28
	s_cselect_b32 s55, s25, s53
	s_cselect_b32 s54, s24, s31
	s_cselect_b32 s57, s4, s29
	s_cselect_b32 s56, s5, s28
	s_mov_b32 m0, s23
	ds_read_b128 v[180:183], v163
	ds_read_b128 v[190:193], v163 offset:1024
	ds_read_b128 v[194:197], v163 offset:2048
	ds_read_b128 v[198:201], v163 offset:3072
	ds_read_b128 v[202:205], v163 offset:4096
	ds_read_b128 v[206:209], v163 offset:5120
	ds_read_b128 v[216:219], v163 offset:6144
	ds_read_b128 v[220:223], v163 offset:7168
	global_load_lds_dwordx4 v138, s[10:11]
	s_mov_b32 m0, s33
	s_nop 0
	s_add_u32 s70, s10, s96
	s_addc_u32 s71, s11, s97
	global_load_lds_dwordx4 v138, s[70:71]
	s_waitcnt vmcnt(8)
	s_waitcnt lgkmcnt(0)
	s_barrier
	v_mfma_f32_16x16x32_bf16 v[120:123], v[144:147], v[180:183], v[120:123]
	v_mfma_f32_16x16x32_bf16 v[120:123], v[148:151], v[190:193], v[120:123]
	v_mfma_f32_16x16x32_bf16 v[116:119], v[152:155], v[180:183], v[116:119]
	v_mfma_f32_16x16x32_bf16 v[116:119], v[156:159], v[190:193], v[116:119]
	v_mfma_f32_16x16x32_bf16 v[128:131], v[164:167], v[180:183], v[128:131]
	v_mfma_f32_16x16x32_bf16 v[128:131], v[168:171], v[190:193], v[128:131]
	v_mfma_f32_16x16x32_bf16 v[124:127], v[172:175], v[180:183], v[124:127]
	v_mfma_f32_16x16x32_bf16 v[124:127], v[176:179], v[190:193], v[124:127]
	v_mfma_f32_16x16x32_bf16 v[104:107], v[144:147], v[194:197], v[104:107]
	v_mfma_f32_16x16x32_bf16 v[104:107], v[148:151], v[198:201], v[104:107]
	v_mfma_f32_16x16x32_bf16 v[100:103], v[152:155], v[194:197], v[100:103]
	v_mfma_f32_16x16x32_bf16 v[100:103], v[156:159], v[198:201], v[100:103]
	v_mfma_f32_16x16x32_bf16 v[112:115], v[164:167], v[194:197], v[112:115]
	v_mfma_f32_16x16x32_bf16 v[112:115], v[168:171], v[198:201], v[112:115]
	v_mfma_f32_16x16x32_bf16 v[108:111], v[172:175], v[194:197], v[108:111]
	v_mfma_f32_16x16x32_bf16 v[108:111], v[176:179], v[198:201], v[108:111]
	v_mfma_f32_16x16x32_bf16 v[88:91], v[144:147], v[202:205], v[88:91]
	v_mfma_f32_16x16x32_bf16 v[88:91], v[148:151], v[206:209], v[88:91]
	v_mfma_f32_16x16x32_bf16 v[84:87], v[152:155], v[202:205], v[84:87]
	v_mfma_f32_16x16x32_bf16 v[84:87], v[156:159], v[206:209], v[84:87]
	v_mfma_f32_16x16x32_bf16 v[96:99], v[164:167], v[202:205], v[96:99]
	v_mfma_f32_16x16x32_bf16 v[96:99], v[168:171], v[206:209], v[96:99]
	v_mfma_f32_16x16x32_bf16 v[92:95], v[172:175], v[202:205], v[92:95]
	v_mfma_f32_16x16x32_bf16 v[92:95], v[176:179], v[206:209], v[92:95]
	v_mfma_f32_16x16x32_bf16 v[72:75], v[144:147], v[216:219], v[72:75]
	v_mfma_f32_16x16x32_bf16 v[72:75], v[148:151], v[220:223], v[72:75]
	v_mfma_f32_16x16x32_bf16 v[68:71], v[152:155], v[216:219], v[68:71]
	v_mfma_f32_16x16x32_bf16 v[68:71], v[156:159], v[220:223], v[68:71]
	v_mfma_f32_16x16x32_bf16 v[80:83], v[164:167], v[216:219], v[80:83]
	v_mfma_f32_16x16x32_bf16 v[80:83], v[168:171], v[220:223], v[80:83]
	v_mfma_f32_16x16x32_bf16 v[76:79], v[172:175], v[216:219], v[76:79]
	v_mfma_f32_16x16x32_bf16 v[76:79], v[176:179], v[220:223], v[76:79]
	s_barrier
	s_mov_b32 m0, s45
	ds_read_b128 v[180:183], v163 offset:16384
	ds_read_b128 v[190:193], v163 offset:17408
	ds_read_b128 v[194:197], v163 offset:18432
	ds_read_b128 v[198:201], v163 offset:19456
	ds_read_b128 v[202:205], v163 offset:20480
	ds_read_b128 v[206:209], v163 offset:21504
	ds_read_b128 v[216:219], v163 offset:22528
	ds_read_b128 v[220:223], v163 offset:23552
	global_load_lds_dwordx4 v132, s[56:57]
	s_mov_b32 m0, s46
	s_nop 0
	s_add_u32 s70, s56, s90
	s_addc_u32 s71, s57, s91
	global_load_lds_dwordx4 v132, s[70:71]
	s_mov_b32 m0, s47
	s_nop 0
	s_add_u32 s70, s56, s60
	s_addc_u32 s71, s57, s61
	global_load_lds_dwordx4 v132, s[70:71]
	s_mov_b32 m0, s48
	s_nop 0
	s_add_u32 s70, s56, s64
	s_addc_u32 s71, s57, s65
	global_load_lds_dwordx4 v132, s[70:71]
	s_mov_b32 m0, s37
	s_nop 0
	global_load_lds_dwordx4 v134, s[54:55]
	s_mov_b32 m0, s38
	s_nop 0
	s_add_u32 s70, s54, s96
	s_addc_u32 s71, s55, s97
	global_load_lds_dwordx4 v134, s[70:71]
	s_waitcnt vmcnt(8)
	s_waitcnt lgkmcnt(0)
	s_barrier
	v_mfma_f32_16x16x32_bf16 v[56:59], v[144:147], v[180:183], v[56:59]
	v_mfma_f32_16x16x32_bf16 v[56:59], v[148:151], v[190:193], v[56:59]
	v_mfma_f32_16x16x32_bf16 v[52:55], v[152:155], v[180:183], v[52:55]
	v_mfma_f32_16x16x32_bf16 v[52:55], v[156:159], v[190:193], v[52:55]
	v_mfma_f32_16x16x32_bf16 v[64:67], v[164:167], v[180:183], v[64:67]
	v_mfma_f32_16x16x32_bf16 v[64:67], v[168:171], v[190:193], v[64:67]
	v_mfma_f32_16x16x32_bf16 v[60:63], v[172:175], v[180:183], v[60:63]
	v_mfma_f32_16x16x32_bf16 v[60:63], v[176:179], v[190:193], v[60:63]
	v_mfma_f32_16x16x32_bf16 v[40:43], v[144:147], v[194:197], v[40:43]
	v_mfma_f32_16x16x32_bf16 v[40:43], v[148:151], v[198:201], v[40:43]
	v_mfma_f32_16x16x32_bf16 v[36:39], v[152:155], v[194:197], v[36:39]
	v_mfma_f32_16x16x32_bf16 v[36:39], v[156:159], v[198:201], v[36:39]
	v_mfma_f32_16x16x32_bf16 v[48:51], v[164:167], v[194:197], v[48:51]
	v_mfma_f32_16x16x32_bf16 v[48:51], v[168:171], v[198:201], v[48:51]
	v_mfma_f32_16x16x32_bf16 v[44:47], v[172:175], v[194:197], v[44:47]
	v_mfma_f32_16x16x32_bf16 v[44:47], v[176:179], v[198:201], v[44:47]
	v_mfma_f32_16x16x32_bf16 v[24:27], v[144:147], v[202:205], v[24:27]
	v_mfma_f32_16x16x32_bf16 v[24:27], v[148:151], v[206:209], v[24:27]
	v_mfma_f32_16x16x32_bf16 v[20:23], v[152:155], v[202:205], v[20:23]
	v_mfma_f32_16x16x32_bf16 v[20:23], v[156:159], v[206:209], v[20:23]
	v_mfma_f32_16x16x32_bf16 v[32:35], v[164:167], v[202:205], v[32:35]
	v_mfma_f32_16x16x32_bf16 v[32:35], v[168:171], v[206:209], v[32:35]
	v_mfma_f32_16x16x32_bf16 v[28:31], v[172:175], v[202:205], v[28:31]
	v_mfma_f32_16x16x32_bf16 v[28:31], v[176:179], v[206:209], v[28:31]
	v_mfma_f32_16x16x32_bf16 v[8:11], v[144:147], v[216:219], v[8:11]
	v_mfma_f32_16x16x32_bf16 v[8:11], v[148:151], v[220:223], v[8:11]
	v_mfma_f32_16x16x32_bf16 v[4:7], v[152:155], v[216:219], v[4:7]
	v_mfma_f32_16x16x32_bf16 v[4:7], v[156:159], v[220:223], v[4:7]
	v_mfma_f32_16x16x32_bf16 v[16:19], v[164:167], v[216:219], v[16:19]
	v_mfma_f32_16x16x32_bf16 v[16:19], v[168:171], v[220:223], v[16:19]
	v_mfma_f32_16x16x32_bf16 v[12:15], v[172:175], v[216:219], v[12:15]
	v_mfma_f32_16x16x32_bf16 v[12:15], v[176:179], v[220:223], v[12:15]
	s_barrier
; #define PG8_MMA(ai, bj, At, Bt) do { __builtin_amdgcn_s_setprio(1); _Pragma("unroll") for (int m = 0; m < 4; ++m) _Pragma("unroll") for (int n = 0; n < 2; ++n) _Pragma("unroll") for (int k = 0; k < 2; ++k) \
;         acc[ai][bj][m][n] = __builtin_amdgcn_mfma_f32_16x16x32_bf16(Bt[n][k], At[m][k], acc[ai][bj][m][n], 0, 0, 0); __builtin_amdgcn_s_setprio(0); } while (0)
; #define PG8_WAIT_V(n) asm volatile("s_waitcnt vmcnt(" #n ")" ::: "memory")
; #define PG8_TRIP_HEAD(T) const int t = (T); const bool last = (t == nt - 2); \
;             const char* a1 = cA + (size_t)(t + 1) * kstep; \
;             const char* a2 = last ? nA : cA + (size_t)(t + 2) * kstep; const char* b2 = last ? nB : cB + (size_t)(t + 2) * kstep; \
;             const char* a3 = a2 + kstep; const char* b3 = b2 + kstep; \
;             if (last && has_next) S.a_ready(nxt);
; template <class Epi, class Sched, bool ALIGN_EPI = false, bool SP2 = false>
; __device__ __forceinline__ void gemm_phase(PG8_LAS unsigned char* lds, const Gemm g, const Sched& S, const Epi& E) {
;     ...
;         if constexpr (SP2) {
;             { PG8_TRIP_HEAD(0) PG8_TRIP_SP2(asm volatile("s_waitcnt vmcnt(%0)" :: "n"(8 + Epi::NST) : "memory"), PG8_MMAZ) }
;             for (int tt = 2; tt < nt; tt += 2) { PG8_TRIP_HEAD(tt) PG8_TRIP_SP2(PG8_WAIT_V(8), PG8_MMA) }
	ds_read_b128 v[144:147], v142
	ds_read_b128 v[148:151], v142 offset:1024
	ds_read_b128 v[152:155], v142 offset:2048
	ds_read_b128 v[156:159], v142 offset:3072
	ds_read_b128 v[164:167], v143
	ds_read_b128 v[168:171], v143 offset:1024
	ds_read_b128 v[172:175], v143 offset:2048
	ds_read_b128 v[176:179], v143 offset:3072
	s_mov_b32 m0, s39
	ds_read_b128 v[180:183], v163 offset:32768
	ds_read_b128 v[190:193], v163 offset:33792
	ds_read_b128 v[194:197], v163 offset:34816
	ds_read_b128 v[198:201], v163 offset:35840
	ds_read_b128 v[202:205], v163 offset:36864
	ds_read_b128 v[206:209], v163 offset:37888
	ds_read_b128 v[216:219], v163 offset:38912
	ds_read_b128 v[220:223], v163 offset:39936
	s_add_u32 s70, s54, s82
	s_addc_u32 s71, s55, s83
	global_load_lds_dwordx4 v134, s[70:71]
	s_mov_b32 m0, s40
	s_nop 0
	s_add_u32 s70, s54, s68
	s_addc_u32 s71, s55, s69
	global_load_lds_dwordx4 v134, s[70:71]
	s_waitcnt vmcnt(8)
	s_waitcnt lgkmcnt(0)
	s_barrier
	v_mfma_f32_16x16x32_bf16 v[120:123], v[144:147], v[180:183], v[120:123]
	v_mfma_f32_16x16x32_bf16 v[120:123], v[148:151], v[190:193], v[120:123]
	v_mfma_f32_16x16x32_bf16 v[116:119], v[152:155], v[180:183], v[116:119]
	v_mfma_f32_16x16x32_bf16 v[116:119], v[156:159], v[190:193], v[116:119]
	v_mfma_f32_16x16x32_bf16 v[128:131], v[164:167], v[180:183], v[128:131]
	v_mfma_f32_16x16x32_bf16 v[128:131], v[168:171], v[190:193], v[128:131]
	v_mfma_f32_16x16x32_bf16 v[124:127], v[172:175], v[180:183], v[124:127]
	v_mfma_f32_16x16x32_bf16 v[124:127], v[176:179], v[190:193], v[124:127]
	v_mfma_f32_16x16x32_bf16 v[104:107], v[144:147], v[194:197], v[104:107]
	v_mfma_f32_16x16x32_bf16 v[104:107], v[148:151], v[198:201], v[104:107]
	v_mfma_f32_16x16x32_bf16 v[100:103], v[152:155], v[194:197], v[100:103]
	v_mfma_f32_16x16x32_bf16 v[100:103], v[156:159], v[198:201], v[100:103]
	v_mfma_f32_16x16x32_bf16 v[112:115], v[164:167], v[194:197], v[112:115]
	v_mfma_f32_16x16x32_bf16 v[112:115], v[168:171], v[198:201], v[112:115]
	v_mfma_f32_16x16x32_bf16 v[108:111], v[172:175], v[194:197], v[108:111]
	v_mfma_f32_16x16x32_bf16 v[108:111], v[176:179], v[198:201], v[108:111]
	v_mfma_f32_16x16x32_bf16 v[88:91], v[144:147], v[202:205], v[88:91]
	v_mfma_f32_16x16x32_bf16 v[88:91], v[148:151], v[206:209], v[88:91]
	v_mfma_f32_16x16x32_bf16 v[84:87], v[152:155], v[202:205], v[84:87]
	v_mfma_f32_16x16x32_bf16 v[84:87], v[156:159], v[206:209], v[84:87]
	v_mfma_f32_16x16x32_bf16 v[96:99], v[164:167], v[202:205], v[96:99]
	v_mfma_f32_16x16x32_bf16 v[96:99], v[168:171], v[206:209], v[96:99]
	v_mfma_f32_16x16x32_bf16 v[92:95], v[172:175], v[202:205], v[92:95]
	v_mfma_f32_16x16x32_bf16 v[92:95], v[176:179], v[206:209], v[92:95]
	v_mfma_f32_16x16x32_bf16 v[72:75], v[144:147], v[216:219], v[72:75]
	v_mfma_f32_16x16x32_bf16 v[72:75], v[148:151], v[220:223], v[72:75]
	v_mfma_f32_16x16x32_bf16 v[68:71], v[152:155], v[216:219], v[68:71]
	v_mfma_f32_16x16x32_bf16 v[68:71], v[156:159], v[220:223], v[68:71]
	v_mfma_f32_16x16x32_bf16 v[80:83], v[164:167], v[216:219], v[80:83]
	v_mfma_f32_16x16x32_bf16 v[80:83], v[168:171], v[220:223], v[80:83]
	v_mfma_f32_16x16x32_bf16 v[76:79], v[172:175], v[216:219], v[76:79]
	v_mfma_f32_16x16x32_bf16 v[76:79], v[176:179], v[220:223], v[76:79]
	s_barrier
	s_mov_b32 m0, s49
	ds_read_b128 v[180:183], v163 offset:49152
	ds_read_b128 v[190:193], v163 offset:50176
	ds_read_b128 v[194:197], v163 offset:51200
	ds_read_b128 v[198:201], v163 offset:52224
	ds_read_b128 v[202:205], v163 offset:53248
	ds_read_b128 v[206:209], v163 offset:54272
	ds_read_b128 v[216:219], v163 offset:55296
	ds_read_b128 v[220:223], v163 offset:56320
	s_add_u32 s70, s56, s78
	s_addc_u32 s71, s57, s79
	global_load_lds_dwordx4 v132, s[70:71]
	s_mov_b32 m0, s50
	s_nop 0
	s_add_u32 s70, s56, s84
	s_addc_u32 s71, s57, s85
	global_load_lds_dwordx4 v132, s[70:71]
	s_mov_b32 m0, s51
	s_add_u32 s70, s56, s62
	s_addc_u32 s71, s57, s63
	global_load_lds_dwordx4 v132, s[70:71]
	s_mov_b32 m0, s52
	s_nop 0
	s_add_u32 s70, s56, s66
	s_addc_u32 s71, s57, s67
	global_load_lds_dwordx4 v132, s[70:71]
	s_mov_b32 m0, s0
	s_nop 0
	s_add_u32 s70, s54, s78
	s_addc_u32 s71, s55, s79
	global_load_lds_dwordx4 v134, s[70:71]
	s_mov_b32 m0, s41
	s_nop 0
	s_add_u32 s70, s54, s92
	s_addc_u32 s71, s55, s93
	global_load_lds_dwordx4 v134, s[70:71]
	s_waitcnt vmcnt(8)
	s_waitcnt lgkmcnt(0)
	s_barrier
	v_mfma_f32_16x16x32_bf16 v[56:59], v[144:147], v[180:183], v[56:59]
	v_mfma_f32_16x16x32_bf16 v[56:59], v[148:151], v[190:193], v[56:59]
	v_mfma_f32_16x16x32_bf16 v[52:55], v[152:155], v[180:183], v[52:55]
	v_mfma_f32_16x16x32_bf16 v[52:55], v[156:159], v[190:193], v[52:55]
	v_mfma_f32_16x16x32_bf16 v[64:67], v[164:167], v[180:183], v[64:67]
	v_mfma_f32_16x16x32_bf16 v[64:67], v[168:171], v[190:193], v[64:67]
	v_mfma_f32_16x16x32_bf16 v[60:63], v[172:175], v[180:183], v[60:63]
	v_mfma_f32_16x16x32_bf16 v[60:63], v[176:179], v[190:193], v[60:63]
	v_mfma_f32_16x16x32_bf16 v[40:43], v[144:147], v[194:197], v[40:43]
	v_mfma_f32_16x16x32_bf16 v[40:43], v[148:151], v[198:201], v[40:43]
	v_mfma_f32_16x16x32_bf16 v[36:39], v[152:155], v[194:197], v[36:39]
	v_mfma_f32_16x16x32_bf16 v[36:39], v[156:159], v[198:201], v[36:39]
	v_mfma_f32_16x16x32_bf16 v[48:51], v[164:167], v[194:197], v[48:51]
	v_mfma_f32_16x16x32_bf16 v[48:51], v[168:171], v[198:201], v[48:51]
	v_mfma_f32_16x16x32_bf16 v[44:47], v[172:175], v[194:197], v[44:47]
	v_mfma_f32_16x16x32_bf16 v[44:47], v[176:179], v[198:201], v[44:47]
	v_mfma_f32_16x16x32_bf16 v[24:27], v[144:147], v[202:205], v[24:27]
	v_mfma_f32_16x16x32_bf16 v[24:27], v[148:151], v[206:209], v[24:27]
	v_mfma_f32_16x16x32_bf16 v[20:23], v[152:155], v[202:205], v[20:23]
	v_mfma_f32_16x16x32_bf16 v[20:23], v[156:159], v[206:209], v[20:23]
	v_mfma_f32_16x16x32_bf16 v[32:35], v[164:167], v[202:205], v[32:35]
	v_mfma_f32_16x16x32_bf16 v[32:35], v[168:171], v[206:209], v[32:35]
	v_mfma_f32_16x16x32_bf16 v[28:31], v[172:175], v[202:205], v[28:31]
	v_mfma_f32_16x16x32_bf16 v[28:31], v[176:179], v[206:209], v[28:31]
	v_mfma_f32_16x16x32_bf16 v[8:11], v[144:147], v[216:219], v[8:11]
	v_mfma_f32_16x16x32_bf16 v[8:11], v[148:151], v[220:223], v[8:11]
	v_mfma_f32_16x16x32_bf16 v[4:7], v[152:155], v[216:219], v[4:7]
	v_mfma_f32_16x16x32_bf16 v[4:7], v[156:159], v[220:223], v[4:7]
	v_mfma_f32_16x16x32_bf16 v[16:19], v[164:167], v[216:219], v[16:19]
	v_mfma_f32_16x16x32_bf16 v[16:19], v[168:171], v[220:223], v[16:19]
	v_mfma_f32_16x16x32_bf16 v[12:15], v[172:175], v[216:219], v[12:15]
	v_mfma_f32_16x16x32_bf16 v[12:15], v[176:179], v[220:223], v[12:15]
	s_barrier
	s_add_i32 s30, s30, 2
	s_add_u32 s10, s10, 0x100
	s_addc_u32 s11, s11, 0
	s_add_u32 s28, s28, 0x100
	s_addc_u32 s29, s29, 0
	s_cmp_gt_u32 s30, 29
	s_cbranch_scc0 .LBB0_130
	s_and_b64 vcc, exec, s[20:21]
	s_cbranch_vccz .LBB0_133
	s_barrier

.LBB0_233:
	ds_read_b128 v[120:123], v116
	ds_read_b128 v[132:135], v116 offset:1024
	ds_read_b128 v[144:147], v116 offset:2048
	ds_read_b128 v[148:151], v116 offset:3072
	ds_read_b128 v[152:155], v117
	ds_read_b128 v[156:159], v117 offset:1024
	ds_read_b128 v[166:169], v117 offset:2048
	ds_read_b128 v[170:173], v117 offset:3072
	s_add_u32 s49, s26, 0xffea0080
	s_addc_u32 s50, s27, -1
	s_cmpk_eq_i32 s48, 0x54
	s_cselect_b32 s51, s21, s50
	s_cselect_b32 s50, s20, s49
	s_cselect_b32 s53, s23, s25
	s_cselect_b32 s52, s22, s24
	s_mov_b32 m0, s0
	ds_read_b128 v[180:183], v178
	ds_read_b128 v[184:187], v178 offset:1024
	ds_read_b128 v[190:193], v178 offset:2048
	ds_read_b128 v[194:197], v178 offset:3072
	ds_read_b128 v[198:201], v178 offset:4096
	ds_read_b128 v[202:205], v178 offset:5120
	ds_read_b128 v[206:209], v178 offset:6144
	ds_read_b128 v[216:219], v178 offset:7168
	global_load_lds_dwordx4 v164, s[26:27]
	s_mov_b32 m0, s4
	s_nop 0
	s_add_u32 s70, s26, s86
	s_addc_u32 s71, s27, s87
	global_load_lds_dwordx4 v164, s[70:71]
	s_waitcnt vmcnt(8)
	s_waitcnt lgkmcnt(0)
	s_barrier
	v_mfma_f32_16x16x32_bf16 v[140:143], v[120:123], v[180:183], v[140:143]
	v_mfma_f32_16x16x32_bf16 v[140:143], v[132:135], v[184:187], v[140:143]
	v_mfma_f32_16x16x32_bf16 v[136:139], v[144:147], v[180:183], v[136:139]
	v_mfma_f32_16x16x32_bf16 v[136:139], v[148:151], v[184:187], v[136:139]
	v_mfma_f32_16x16x32_bf16 v[128:131], v[152:155], v[180:183], v[128:131]
	v_mfma_f32_16x16x32_bf16 v[128:131], v[156:159], v[184:187], v[128:131]
	v_mfma_f32_16x16x32_bf16 v[124:127], v[166:169], v[180:183], v[124:127]
	v_mfma_f32_16x16x32_bf16 v[124:127], v[170:173], v[184:187], v[124:127]
	v_mfma_f32_16x16x32_bf16 v[112:115], v[120:123], v[190:193], v[112:115]
	v_mfma_f32_16x16x32_bf16 v[112:115], v[132:135], v[194:197], v[112:115]
	v_mfma_f32_16x16x32_bf16 v[108:111], v[144:147], v[190:193], v[108:111]
	v_mfma_f32_16x16x32_bf16 v[108:111], v[148:151], v[194:197], v[108:111]
	v_mfma_f32_16x16x32_bf16 v[104:107], v[152:155], v[190:193], v[104:107]
	v_mfma_f32_16x16x32_bf16 v[104:107], v[156:159], v[194:197], v[104:107]
	v_mfma_f32_16x16x32_bf16 v[100:103], v[166:169], v[190:193], v[100:103]
	v_mfma_f32_16x16x32_bf16 v[100:103], v[170:173], v[194:197], v[100:103]
	v_mfma_f32_16x16x32_bf16 v[96:99], v[120:123], v[198:201], v[96:99]
	v_mfma_f32_16x16x32_bf16 v[96:99], v[132:135], v[202:205], v[96:99]
	v_mfma_f32_16x16x32_bf16 v[92:95], v[144:147], v[198:201], v[92:95]
	v_mfma_f32_16x16x32_bf16 v[92:95], v[148:151], v[202:205], v[92:95]
	v_mfma_f32_16x16x32_bf16 v[88:91], v[152:155], v[198:201], v[88:91]
	v_mfma_f32_16x16x32_bf16 v[88:91], v[156:159], v[202:205], v[88:91]
	v_mfma_f32_16x16x32_bf16 v[84:87], v[166:169], v[198:201], v[84:87]
	v_mfma_f32_16x16x32_bf16 v[84:87], v[170:173], v[202:205], v[84:87]
	v_mfma_f32_16x16x32_bf16 v[80:83], v[120:123], v[206:209], v[80:83]
	v_mfma_f32_16x16x32_bf16 v[80:83], v[132:135], v[216:219], v[80:83]
	v_mfma_f32_16x16x32_bf16 v[76:79], v[144:147], v[206:209], v[76:79]
	v_mfma_f32_16x16x32_bf16 v[76:79], v[148:151], v[216:219], v[76:79]
	v_mfma_f32_16x16x32_bf16 v[72:75], v[152:155], v[206:209], v[72:75]
	v_mfma_f32_16x16x32_bf16 v[72:75], v[156:159], v[216:219], v[72:75]
	v_mfma_f32_16x16x32_bf16 v[68:71], v[166:169], v[206:209], v[68:71]
	v_mfma_f32_16x16x32_bf16 v[68:71], v[170:173], v[216:219], v[68:71]
	s_barrier
	s_mov_b32 m0, s5
	ds_read_b128 v[180:183], v178 offset:16384
	ds_read_b128 v[184:187], v178 offset:17408
	ds_read_b128 v[190:193], v178 offset:18432
	ds_read_b128 v[194:197], v178 offset:19456
	ds_read_b128 v[198:201], v178 offset:20480
	ds_read_b128 v[202:205], v178 offset:21504
	ds_read_b128 v[206:209], v178 offset:22528
	ds_read_b128 v[216:219], v178 offset:23552
	global_load_lds_dwordx4 v162, s[52:53]
	s_mov_b32 m0, s33
	s_nop 0
	s_add_u32 s70, s52, s86
	s_addc_u32 s71, s53, s87
	global_load_lds_dwordx4 v162, s[70:71]
	s_mov_b32 m0, s42
	s_nop 0
	s_add_u32 s70, s52, s54
	s_addc_u32 s71, s53, s55
	global_load_lds_dwordx4 v162, s[70:71]
	s_mov_b32 m0, s43
	s_nop 0
	s_add_u32 s70, s52, s56
	s_addc_u32 s71, s53, s57
	global_load_lds_dwordx4 v162, s[70:71]
	s_mov_b32 m0, s31
	s_nop 0
	global_load_lds_dwordx4 v160, s[50:51]
	s_mov_b32 m0, s34
	s_nop 0
	s_add_u32 s70, s50, s86
	s_addc_u32 s71, s51, s87
	global_load_lds_dwordx4 v160, s[70:71]
	s_waitcnt vmcnt(8)
	s_waitcnt lgkmcnt(0)
	s_barrier
	v_mfma_f32_16x16x32_bf16 v[56:59], v[120:123], v[180:183], v[56:59]
	v_mfma_f32_16x16x32_bf16 v[56:59], v[132:135], v[184:187], v[56:59]
	v_mfma_f32_16x16x32_bf16 v[52:55], v[144:147], v[180:183], v[52:55]
	v_mfma_f32_16x16x32_bf16 v[52:55], v[148:151], v[184:187], v[52:55]
	v_mfma_f32_16x16x32_bf16 v[64:67], v[152:155], v[180:183], v[64:67]
	v_mfma_f32_16x16x32_bf16 v[64:67], v[156:159], v[184:187], v[64:67]
	v_mfma_f32_16x16x32_bf16 v[60:63], v[166:169], v[180:183], v[60:63]
	v_mfma_f32_16x16x32_bf16 v[60:63], v[170:173], v[184:187], v[60:63]
	v_mfma_f32_16x16x32_bf16 v[48:51], v[120:123], v[190:193], v[48:51]
	v_mfma_f32_16x16x32_bf16 v[48:51], v[132:135], v[194:197], v[48:51]
	v_mfma_f32_16x16x32_bf16 v[44:47], v[144:147], v[190:193], v[44:47]
	v_mfma_f32_16x16x32_bf16 v[44:47], v[148:151], v[194:197], v[44:47]
	v_mfma_f32_16x16x32_bf16 v[40:43], v[152:155], v[190:193], v[40:43]
	v_mfma_f32_16x16x32_bf16 v[40:43], v[156:159], v[194:197], v[40:43]
	v_mfma_f32_16x16x32_bf16 v[36:39], v[166:169], v[190:193], v[36:39]
	v_mfma_f32_16x16x32_bf16 v[36:39], v[170:173], v[194:197], v[36:39]
	v_mfma_f32_16x16x32_bf16 v[32:35], v[120:123], v[198:201], v[32:35]
	v_mfma_f32_16x16x32_bf16 v[32:35], v[132:135], v[202:205], v[32:35]
	v_mfma_f32_16x16x32_bf16 v[28:31], v[144:147], v[198:201], v[28:31]
	v_mfma_f32_16x16x32_bf16 v[28:31], v[148:151], v[202:205], v[28:31]
	v_mfma_f32_16x16x32_bf16 v[24:27], v[152:155], v[198:201], v[24:27]
	v_mfma_f32_16x16x32_bf16 v[24:27], v[156:159], v[202:205], v[24:27]
	v_mfma_f32_16x16x32_bf16 v[20:23], v[166:169], v[198:201], v[20:23]
	v_mfma_f32_16x16x32_bf16 v[20:23], v[170:173], v[202:205], v[20:23]
	v_mfma_f32_16x16x32_bf16 v[16:19], v[120:123], v[206:209], v[16:19]
	v_mfma_f32_16x16x32_bf16 v[16:19], v[132:135], v[216:219], v[16:19]
	v_mfma_f32_16x16x32_bf16 v[12:15], v[144:147], v[206:209], v[12:15]
	v_mfma_f32_16x16x32_bf16 v[12:15], v[148:151], v[216:219], v[12:15]
	v_mfma_f32_16x16x32_bf16 v[8:11], v[152:155], v[206:209], v[8:11]
	v_mfma_f32_16x16x32_bf16 v[8:11], v[156:159], v[216:219], v[8:11]
	v_mfma_f32_16x16x32_bf16 v[4:7], v[166:169], v[206:209], v[4:7]
	v_mfma_f32_16x16x32_bf16 v[4:7], v[170:173], v[216:219], v[4:7]
	s_barrier
; #define PG8_MMA(ai, bj, At, Bt) do { __builtin_amdgcn_s_setprio(1); _Pragma("unroll") for (int m = 0; m < 4; ++m) _Pragma("unroll") for (int n = 0; n < 2; ++n) _Pragma("unroll") for (int k = 0; k < 2; ++k) \
;         acc[ai][bj][m][n] = __builtin_amdgcn_mfma_f32_16x16x32_bf16(Bt[n][k], At[m][k], acc[ai][bj][m][n], 0, 0, 0); __builtin_amdgcn_s_setprio(0); } while (0)
; #define PG8_WAIT_V(n) asm volatile("s_waitcnt vmcnt(" #n ")" ::: "memory")
; #define PG8_TRIP_HEAD(T) const int t = (T); const bool last = (t == nt - 2); \
;             const char* a1 = cA + (size_t)(t + 1) * kstep; \
;             const char* a2 = last ? nA : cA + (size_t)(t + 2) * kstep; const char* b2 = last ? nB : cB + (size_t)(t + 2) * kstep; \
;             const char* a3 = a2 + kstep; const char* b3 = b2 + kstep; \
;             if (last && has_next) S.a_ready(nxt);
; template <class Epi, class Sched, bool ALIGN_EPI = false, bool SP2 = false>
; __device__ __forceinline__ void gemm_phase(PG8_LAS unsigned char* lds, const Gemm g, const Sched& S, const Epi& E) {
;     ...
;         if constexpr (SP2) {
;             { PG8_TRIP_HEAD(0) PG8_TRIP_SP2(asm volatile("s_waitcnt vmcnt(%0)" :: "n"(8 + Epi::NST) : "memory"), PG8_MMAZ) }
;             for (int tt = 2; tt < nt; tt += 2) { PG8_TRIP_HEAD(tt) PG8_TRIP_SP2(PG8_WAIT_V(8), PG8_MMA) }
	ds_read_b128 v[120:123], v118
	ds_read_b128 v[132:135], v118 offset:1024
	ds_read_b128 v[144:147], v118 offset:2048
	ds_read_b128 v[148:151], v118 offset:3072
	ds_read_b128 v[152:155], v119
	ds_read_b128 v[156:159], v119 offset:1024
	ds_read_b128 v[166:169], v119 offset:2048
	ds_read_b128 v[170:173], v119 offset:3072
	s_mov_b32 m0, s35
	ds_read_b128 v[180:183], v178 offset:32768
	ds_read_b128 v[184:187], v178 offset:33792
	ds_read_b128 v[190:193], v178 offset:34816
	ds_read_b128 v[194:197], v178 offset:35840
	ds_read_b128 v[198:201], v178 offset:36864
	ds_read_b128 v[202:205], v178 offset:37888
	ds_read_b128 v[206:209], v178 offset:38912
	ds_read_b128 v[216:219], v178 offset:39936
	s_add_u32 s70, s50, s54
	s_addc_u32 s71, s51, s55
	global_load_lds_dwordx4 v160, s[70:71]
	s_mov_b32 m0, s36
	s_nop 0
	s_add_u32 s70, s50, s56
	s_addc_u32 s71, s51, s57
	global_load_lds_dwordx4 v160, s[70:71]
	s_waitcnt vmcnt(8)
	s_waitcnt lgkmcnt(0)
	s_barrier
	v_mfma_f32_16x16x32_bf16 v[140:143], v[120:123], v[180:183], v[140:143]
	v_mfma_f32_16x16x32_bf16 v[140:143], v[132:135], v[184:187], v[140:143]
	v_mfma_f32_16x16x32_bf16 v[136:139], v[144:147], v[180:183], v[136:139]
	v_mfma_f32_16x16x32_bf16 v[136:139], v[148:151], v[184:187], v[136:139]
	v_mfma_f32_16x16x32_bf16 v[128:131], v[152:155], v[180:183], v[128:131]
	v_mfma_f32_16x16x32_bf16 v[128:131], v[156:159], v[184:187], v[128:131]
	v_mfma_f32_16x16x32_bf16 v[124:127], v[166:169], v[180:183], v[124:127]
	v_mfma_f32_16x16x32_bf16 v[124:127], v[170:173], v[184:187], v[124:127]
	v_mfma_f32_16x16x32_bf16 v[112:115], v[120:123], v[190:193], v[112:115]
	v_mfma_f32_16x16x32_bf16 v[112:115], v[132:135], v[194:197], v[112:115]
	v_mfma_f32_16x16x32_bf16 v[108:111], v[144:147], v[190:193], v[108:111]
	v_mfma_f32_16x16x32_bf16 v[108:111], v[148:151], v[194:197], v[108:111]
	v_mfma_f32_16x16x32_bf16 v[104:107], v[152:155], v[190:193], v[104:107]
	v_mfma_f32_16x16x32_bf16 v[104:107], v[156:159], v[194:197], v[104:107]
	v_mfma_f32_16x16x32_bf16 v[100:103], v[166:169], v[190:193], v[100:103]
	v_mfma_f32_16x16x32_bf16 v[100:103], v[170:173], v[194:197], v[100:103]
	v_mfma_f32_16x16x32_bf16 v[96:99], v[120:123], v[198:201], v[96:99]
	v_mfma_f32_16x16x32_bf16 v[96:99], v[132:135], v[202:205], v[96:99]
	v_mfma_f32_16x16x32_bf16 v[92:95], v[144:147], v[198:201], v[92:95]
	v_mfma_f32_16x16x32_bf16 v[92:95], v[148:151], v[202:205], v[92:95]
	v_mfma_f32_16x16x32_bf16 v[88:91], v[152:155], v[198:201], v[88:91]
	v_mfma_f32_16x16x32_bf16 v[88:91], v[156:159], v[202:205], v[88:91]
	v_mfma_f32_16x16x32_bf16 v[84:87], v[166:169], v[198:201], v[84:87]
	v_mfma_f32_16x16x32_bf16 v[84:87], v[170:173], v[202:205], v[84:87]
	v_mfma_f32_16x16x32_bf16 v[80:83], v[120:123], v[206:209], v[80:83]
	v_mfma_f32_16x16x32_bf16 v[80:83], v[132:135], v[216:219], v[80:83]
	v_mfma_f32_16x16x32_bf16 v[76:79], v[144:147], v[206:209], v[76:79]
	v_mfma_f32_16x16x32_bf16 v[76:79], v[148:151], v[216:219], v[76:79]
	v_mfma_f32_16x16x32_bf16 v[72:75], v[152:155], v[206:209], v[72:75]
	v_mfma_f32_16x16x32_bf16 v[72:75], v[156:159], v[216:219], v[72:75]
	v_mfma_f32_16x16x32_bf16 v[68:71], v[166:169], v[206:209], v[68:71]
	v_mfma_f32_16x16x32_bf16 v[68:71], v[170:173], v[216:219], v[68:71]
	s_barrier
	s_mov_b32 m0, s44
	ds_read_b128 v[180:183], v178 offset:49152
	ds_read_b128 v[184:187], v178 offset:50176
	ds_read_b128 v[190:193], v178 offset:51200
	ds_read_b128 v[194:197], v178 offset:52224
	ds_read_b128 v[198:201], v178 offset:53248
	ds_read_b128 v[202:205], v178 offset:54272
	ds_read_b128 v[206:209], v178 offset:55296
	ds_read_b128 v[216:219], v178 offset:56320
	s_add_u32 s70, s52, s78
	s_addc_u32 s71, s53, s79
	global_load_lds_dwordx4 v162, s[70:71]
	s_mov_b32 m0, s45
	s_nop 0
	s_add_u32 s70, s52, s60
	s_addc_u32 s71, s53, s61
	global_load_lds_dwordx4 v162, s[70:71]
	s_mov_b32 m0, s46
	s_add_u32 s70, s52, s62
	s_addc_u32 s71, s53, s63
	global_load_lds_dwordx4 v162, s[70:71]
	s_mov_b32 m0, s47
	s_nop 0
	s_add_u32 s70, s52, s64
	s_addc_u32 s71, s53, s65
	global_load_lds_dwordx4 v162, s[70:71]
	s_mov_b32 m0, s37
	s_nop 0
	s_add_u32 s70, s50, s78
	s_addc_u32 s71, s51, s79
	global_load_lds_dwordx4 v160, s[70:71]
	s_mov_b32 m0, s38
	s_nop 0
	s_add_u32 s70, s50, s60
	s_addc_u32 s71, s51, s61
	global_load_lds_dwordx4 v160, s[70:71]
	s_waitcnt vmcnt(8)
	s_waitcnt lgkmcnt(0)
	s_barrier
	v_mfma_f32_16x16x32_bf16 v[56:59], v[120:123], v[180:183], v[56:59]
	v_mfma_f32_16x16x32_bf16 v[56:59], v[132:135], v[184:187], v[56:59]
	v_mfma_f32_16x16x32_bf16 v[52:55], v[144:147], v[180:183], v[52:55]
	v_mfma_f32_16x16x32_bf16 v[52:55], v[148:151], v[184:187], v[52:55]
	v_mfma_f32_16x16x32_bf16 v[64:67], v[152:155], v[180:183], v[64:67]
	v_mfma_f32_16x16x32_bf16 v[64:67], v[156:159], v[184:187], v[64:67]
	v_mfma_f32_16x16x32_bf16 v[60:63], v[166:169], v[180:183], v[60:63]
	v_mfma_f32_16x16x32_bf16 v[60:63], v[170:173], v[184:187], v[60:63]
	v_mfma_f32_16x16x32_bf16 v[48:51], v[120:123], v[190:193], v[48:51]
	v_mfma_f32_16x16x32_bf16 v[48:51], v[132:135], v[194:197], v[48:51]
	v_mfma_f32_16x16x32_bf16 v[44:47], v[144:147], v[190:193], v[44:47]
	v_mfma_f32_16x16x32_bf16 v[44:47], v[148:151], v[194:197], v[44:47]
	v_mfma_f32_16x16x32_bf16 v[40:43], v[152:155], v[190:193], v[40:43]
	v_mfma_f32_16x16x32_bf16 v[40:43], v[156:159], v[194:197], v[40:43]
	v_mfma_f32_16x16x32_bf16 v[36:39], v[166:169], v[190:193], v[36:39]
	v_mfma_f32_16x16x32_bf16 v[36:39], v[170:173], v[194:197], v[36:39]
	v_mfma_f32_16x16x32_bf16 v[32:35], v[120:123], v[198:201], v[32:35]
	v_mfma_f32_16x16x32_bf16 v[32:35], v[132:135], v[202:205], v[32:35]
	v_mfma_f32_16x16x32_bf16 v[28:31], v[144:147], v[198:201], v[28:31]
	v_mfma_f32_16x16x32_bf16 v[28:31], v[148:151], v[202:205], v[28:31]
	v_mfma_f32_16x16x32_bf16 v[24:27], v[152:155], v[198:201], v[24:27]
	v_mfma_f32_16x16x32_bf16 v[24:27], v[156:159], v[202:205], v[24:27]
	v_mfma_f32_16x16x32_bf16 v[20:23], v[166:169], v[198:201], v[20:23]
	v_mfma_f32_16x16x32_bf16 v[20:23], v[170:173], v[202:205], v[20:23]
	v_mfma_f32_16x16x32_bf16 v[16:19], v[120:123], v[206:209], v[16:19]
	v_mfma_f32_16x16x32_bf16 v[16:19], v[132:135], v[216:219], v[16:19]
	v_mfma_f32_16x16x32_bf16 v[12:15], v[144:147], v[206:209], v[12:15]
	v_mfma_f32_16x16x32_bf16 v[12:15], v[148:151], v[216:219], v[12:15]
	v_mfma_f32_16x16x32_bf16 v[8:11], v[152:155], v[206:209], v[8:11]
	v_mfma_f32_16x16x32_bf16 v[8:11], v[156:159], v[216:219], v[8:11]
	v_mfma_f32_16x16x32_bf16 v[4:7], v[166:169], v[206:209], v[4:7]
	v_mfma_f32_16x16x32_bf16 v[4:7], v[170:173], v[216:219], v[4:7]
	s_barrier
	s_add_i32 s48, s48, 2
	s_add_u32 s26, s26, 0x100
	s_addc_u32 s27, s27, 0
	s_add_u32 s24, s24, 0x100
	s_addc_u32 s25, s25, 0
	s_cmpk_gt_u32 s48, 0x55
	s_cbranch_scc0 .LBB0_233
	s_and_b64 vcc, exec, s[18:19]
	s_cbranch_vccz .LBB0_236
	s_barrier

.LBB0_324:
	ds_read_b128 v[136:139], v132
	ds_read_b128 v[140:143], v132 offset:1024
	ds_read_b128 v[144:147], v132 offset:2048
	ds_read_b128 v[148:151], v132 offset:3072
	ds_read_b128 v[152:155], v133
	ds_read_b128 v[156:159], v133 offset:1024
	ds_read_b128 v[160:163], v133 offset:2048
	ds_read_b128 v[174:177], v133 offset:3072
	s_add_u32 s15, s10, 0xfff7c080
	s_addc_u32 s50, s11, -1
	s_cmp_eq_u32 s14, 28
	s_cselect_b32 s51, s25, s50
	s_cselect_b32 s50, s24, s15
	s_cselect_b32 s53, s3, s13
	s_cselect_b32 s52, s4, s12
	s_mov_b32 m0, s5
	ds_read_b128 v[178:181], v200
	ds_read_b128 v[182:185], v200 offset:1024
	ds_read_b128 v[186:189], v200 offset:2048
	ds_read_b128 v[190:193], v200 offset:3072
	ds_read_b128 v[202:205], v200 offset:4096
	ds_read_b128 v[206:209], v200 offset:5120
	ds_read_b128 v[216:219], v200 offset:6144
	ds_read_b128 v[220:223], v200 offset:7168
	global_load_lds_dwordx4 v172, s[10:11]
	s_mov_b32 m0, s23
	s_nop 0
	s_add_u32 s70, s10, s96
	s_addc_u32 s71, s11, s97
	global_load_lds_dwordx4 v172, s[70:71]
	s_waitcnt vmcnt(8)
	s_waitcnt lgkmcnt(0)
	s_barrier
	v_mfma_f32_16x16x32_bf16 v[120:123], v[136:139], v[178:181], v[120:123]
	v_mfma_f32_16x16x32_bf16 v[120:123], v[140:143], v[182:185], v[120:123]
	v_mfma_f32_16x16x32_bf16 v[116:119], v[144:147], v[178:181], v[116:119]
	v_mfma_f32_16x16x32_bf16 v[116:119], v[148:151], v[182:185], v[116:119]
	v_mfma_f32_16x16x32_bf16 v[128:131], v[152:155], v[178:181], v[128:131]
	v_mfma_f32_16x16x32_bf16 v[128:131], v[156:159], v[182:185], v[128:131]
	v_mfma_f32_16x16x32_bf16 v[124:127], v[160:163], v[178:181], v[124:127]
	v_mfma_f32_16x16x32_bf16 v[124:127], v[174:177], v[182:185], v[124:127]
	v_mfma_f32_16x16x32_bf16 v[104:107], v[136:139], v[186:189], v[104:107]
	v_mfma_f32_16x16x32_bf16 v[104:107], v[140:143], v[190:193], v[104:107]
	v_mfma_f32_16x16x32_bf16 v[100:103], v[144:147], v[186:189], v[100:103]
	v_mfma_f32_16x16x32_bf16 v[100:103], v[148:151], v[190:193], v[100:103]
	v_mfma_f32_16x16x32_bf16 v[112:115], v[152:155], v[186:189], v[112:115]
	v_mfma_f32_16x16x32_bf16 v[112:115], v[156:159], v[190:193], v[112:115]
	v_mfma_f32_16x16x32_bf16 v[108:111], v[160:163], v[186:189], v[108:111]
	v_mfma_f32_16x16x32_bf16 v[108:111], v[174:177], v[190:193], v[108:111]
	v_mfma_f32_16x16x32_bf16 v[88:91], v[136:139], v[202:205], v[88:91]
	v_mfma_f32_16x16x32_bf16 v[88:91], v[140:143], v[206:209], v[88:91]
	v_mfma_f32_16x16x32_bf16 v[84:87], v[144:147], v[202:205], v[84:87]
	v_mfma_f32_16x16x32_bf16 v[84:87], v[148:151], v[206:209], v[84:87]
	v_mfma_f32_16x16x32_bf16 v[96:99], v[152:155], v[202:205], v[96:99]
	v_mfma_f32_16x16x32_bf16 v[96:99], v[156:159], v[206:209], v[96:99]
	v_mfma_f32_16x16x32_bf16 v[92:95], v[160:163], v[202:205], v[92:95]
	v_mfma_f32_16x16x32_bf16 v[92:95], v[174:177], v[206:209], v[92:95]
	v_mfma_f32_16x16x32_bf16 v[72:75], v[136:139], v[216:219], v[72:75]
	v_mfma_f32_16x16x32_bf16 v[72:75], v[140:143], v[220:223], v[72:75]
	v_mfma_f32_16x16x32_bf16 v[68:71], v[144:147], v[216:219], v[68:71]
	v_mfma_f32_16x16x32_bf16 v[68:71], v[148:151], v[220:223], v[68:71]
	v_mfma_f32_16x16x32_bf16 v[80:83], v[152:155], v[216:219], v[80:83]
	v_mfma_f32_16x16x32_bf16 v[80:83], v[156:159], v[220:223], v[80:83]
	v_mfma_f32_16x16x32_bf16 v[76:79], v[160:163], v[216:219], v[76:79]
	v_mfma_f32_16x16x32_bf16 v[76:79], v[174:177], v[220:223], v[76:79]
	s_barrier
	s_mov_b32 m0, s28
	ds_read_b128 v[178:181], v200 offset:16384
	ds_read_b128 v[182:185], v200 offset:17408
	ds_read_b128 v[186:189], v200 offset:18432
	ds_read_b128 v[190:193], v200 offset:19456
	ds_read_b128 v[202:205], v200 offset:20480
	ds_read_b128 v[206:209], v200 offset:21504
	ds_read_b128 v[216:219], v200 offset:22528
	ds_read_b128 v[220:223], v200 offset:23552
	global_load_lds_dwordx4 v164, s[52:53]
	s_mov_b32 m0, s29
	s_nop 0
	s_add_u32 s70, s52, s90
	s_addc_u32 s71, s53, s91
	global_load_lds_dwordx4 v164, s[70:71]
	s_mov_b32 m0, s33
	s_nop 0
	s_add_u32 s70, s52, s54
	s_addc_u32 s71, s53, s55
	global_load_lds_dwordx4 v164, s[70:71]
	s_mov_b32 m0, s45
	s_nop 0
	s_add_u32 s70, s52, s60
	s_addc_u32 s71, s53, s61
	global_load_lds_dwordx4 v164, s[70:71]
	s_mov_b32 m0, s30
	s_nop 0
	global_load_lds_dwordx4 v166, s[50:51]
	s_mov_b32 m0, s31
	s_nop 0
	s_add_u32 s70, s50, s96
	s_addc_u32 s71, s51, s97
	global_load_lds_dwordx4 v166, s[70:71]
	s_waitcnt vmcnt(8)
	s_waitcnt lgkmcnt(0)
	s_barrier
	v_mfma_f32_16x16x32_bf16 v[56:59], v[136:139], v[178:181], v[56:59]
	v_mfma_f32_16x16x32_bf16 v[56:59], v[140:143], v[182:185], v[56:59]
	v_mfma_f32_16x16x32_bf16 v[52:55], v[144:147], v[178:181], v[52:55]
	v_mfma_f32_16x16x32_bf16 v[52:55], v[148:151], v[182:185], v[52:55]
	v_mfma_f32_16x16x32_bf16 v[64:67], v[152:155], v[178:181], v[64:67]
	v_mfma_f32_16x16x32_bf16 v[64:67], v[156:159], v[182:185], v[64:67]
	v_mfma_f32_16x16x32_bf16 v[60:63], v[160:163], v[178:181], v[60:63]
	v_mfma_f32_16x16x32_bf16 v[60:63], v[174:177], v[182:185], v[60:63]
	v_mfma_f32_16x16x32_bf16 v[40:43], v[136:139], v[186:189], v[40:43]
	v_mfma_f32_16x16x32_bf16 v[40:43], v[140:143], v[190:193], v[40:43]
	v_mfma_f32_16x16x32_bf16 v[36:39], v[144:147], v[186:189], v[36:39]
	v_mfma_f32_16x16x32_bf16 v[36:39], v[148:151], v[190:193], v[36:39]
	v_mfma_f32_16x16x32_bf16 v[48:51], v[152:155], v[186:189], v[48:51]
	v_mfma_f32_16x16x32_bf16 v[48:51], v[156:159], v[190:193], v[48:51]
	v_mfma_f32_16x16x32_bf16 v[44:47], v[160:163], v[186:189], v[44:47]
	v_mfma_f32_16x16x32_bf16 v[44:47], v[174:177], v[190:193], v[44:47]
	v_mfma_f32_16x16x32_bf16 v[24:27], v[136:139], v[202:205], v[24:27]
	v_mfma_f32_16x16x32_bf16 v[24:27], v[140:143], v[206:209], v[24:27]
	v_mfma_f32_16x16x32_bf16 v[20:23], v[144:147], v[202:205], v[20:23]
	v_mfma_f32_16x16x32_bf16 v[20:23], v[148:151], v[206:209], v[20:23]
	v_mfma_f32_16x16x32_bf16 v[32:35], v[152:155], v[202:205], v[32:35]
	v_mfma_f32_16x16x32_bf16 v[32:35], v[156:159], v[206:209], v[32:35]
	v_mfma_f32_16x16x32_bf16 v[28:31], v[160:163], v[202:205], v[28:31]
	v_mfma_f32_16x16x32_bf16 v[28:31], v[174:177], v[206:209], v[28:31]
	v_mfma_f32_16x16x32_bf16 v[8:11], v[136:139], v[216:219], v[8:11]
	v_mfma_f32_16x16x32_bf16 v[8:11], v[140:143], v[220:223], v[8:11]
	v_mfma_f32_16x16x32_bf16 v[4:7], v[144:147], v[216:219], v[4:7]
	v_mfma_f32_16x16x32_bf16 v[4:7], v[148:151], v[220:223], v[4:7]
	v_mfma_f32_16x16x32_bf16 v[16:19], v[152:155], v[216:219], v[16:19]
	v_mfma_f32_16x16x32_bf16 v[16:19], v[156:159], v[220:223], v[16:19]
	v_mfma_f32_16x16x32_bf16 v[12:15], v[160:163], v[216:219], v[12:15]
	v_mfma_f32_16x16x32_bf16 v[12:15], v[174:177], v[220:223], v[12:15]
	s_barrier
; #define PG8_MMA(ai, bj, At, Bt) do { __builtin_amdgcn_s_setprio(1); _Pragma("unroll") for (int m = 0; m < 4; ++m) _Pragma("unroll") for (int n = 0; n < 2; ++n) _Pragma("unroll") for (int k = 0; k < 2; ++k) \
;         acc[ai][bj][m][n] = __builtin_amdgcn_mfma_f32_16x16x32_bf16(Bt[n][k], At[m][k], acc[ai][bj][m][n], 0, 0, 0); __builtin_amdgcn_s_setprio(0); } while (0)
; #define PG8_WAIT_V(n) asm volatile("s_waitcnt vmcnt(" #n ")" ::: "memory")
; #define PG8_TRIP_HEAD(T) const int t = (T); const bool last = (t == nt - 2); \
;             const char* a1 = cA + (size_t)(t + 1) * kstep; \
;             const char* a2 = last ? nA : cA + (size_t)(t + 2) * kstep; const char* b2 = last ? nB : cB + (size_t)(t + 2) * kstep; \
;             const char* a3 = a2 + kstep; const char* b3 = b2 + kstep; \
;             if (last && has_next) S.a_ready(nxt);
; template <class Epi, class Sched, bool ALIGN_EPI = false, bool SP2 = false>
; __device__ __forceinline__ void gemm_phase(PG8_LAS unsigned char* lds, const Gemm g, const Sched& S, const Epi& E) {
;     ...
;         if constexpr (SP2) {
;             { PG8_TRIP_HEAD(0) PG8_TRIP_SP2(asm volatile("s_waitcnt vmcnt(%0)" :: "n"(8 + Epi::NST) : "memory"), PG8_MMAZ) }
;             for (int tt = 2; tt < nt; tt += 2) { PG8_TRIP_HEAD(tt) PG8_TRIP_SP2(PG8_WAIT_V(8), PG8_MMA) }
	ds_read_b128 v[136:139], v134
	ds_read_b128 v[140:143], v134 offset:1024
	ds_read_b128 v[144:147], v134 offset:2048
	ds_read_b128 v[148:151], v134 offset:3072
	ds_read_b128 v[152:155], v135
	ds_read_b128 v[156:159], v135 offset:1024
	ds_read_b128 v[160:163], v135 offset:2048
	ds_read_b128 v[174:177], v135 offset:3072
	s_mov_b32 m0, s34
	ds_read_b128 v[178:181], v200 offset:32768
	ds_read_b128 v[182:185], v200 offset:33792
	ds_read_b128 v[186:189], v200 offset:34816
	ds_read_b128 v[190:193], v200 offset:35840
	ds_read_b128 v[202:205], v200 offset:36864
	ds_read_b128 v[206:209], v200 offset:37888
	ds_read_b128 v[216:219], v200 offset:38912
	ds_read_b128 v[220:223], v200 offset:39936
	s_add_u32 s70, s50, s82
	s_addc_u32 s71, s51, s83
	global_load_lds_dwordx4 v166, s[70:71]
	s_mov_b32 m0, s35
	s_nop 0
	s_add_u32 s70, s50, s64
	s_addc_u32 s71, s51, s65
	global_load_lds_dwordx4 v166, s[70:71]
	s_waitcnt vmcnt(8)
	s_waitcnt lgkmcnt(0)
	s_barrier
	v_mfma_f32_16x16x32_bf16 v[120:123], v[136:139], v[178:181], v[120:123]
	v_mfma_f32_16x16x32_bf16 v[120:123], v[140:143], v[182:185], v[120:123]
	v_mfma_f32_16x16x32_bf16 v[116:119], v[144:147], v[178:181], v[116:119]
	v_mfma_f32_16x16x32_bf16 v[116:119], v[148:151], v[182:185], v[116:119]
	v_mfma_f32_16x16x32_bf16 v[128:131], v[152:155], v[178:181], v[128:131]
	v_mfma_f32_16x16x32_bf16 v[128:131], v[156:159], v[182:185], v[128:131]
	v_mfma_f32_16x16x32_bf16 v[124:127], v[160:163], v[178:181], v[124:127]
	v_mfma_f32_16x16x32_bf16 v[124:127], v[174:177], v[182:185], v[124:127]
	v_mfma_f32_16x16x32_bf16 v[104:107], v[136:139], v[186:189], v[104:107]
	v_mfma_f32_16x16x32_bf16 v[104:107], v[140:143], v[190:193], v[104:107]
	v_mfma_f32_16x16x32_bf16 v[100:103], v[144:147], v[186:189], v[100:103]
	v_mfma_f32_16x16x32_bf16 v[100:103], v[148:151], v[190:193], v[100:103]
	v_mfma_f32_16x16x32_bf16 v[112:115], v[152:155], v[186:189], v[112:115]
	v_mfma_f32_16x16x32_bf16 v[112:115], v[156:159], v[190:193], v[112:115]
	v_mfma_f32_16x16x32_bf16 v[108:111], v[160:163], v[186:189], v[108:111]
	v_mfma_f32_16x16x32_bf16 v[108:111], v[174:177], v[190:193], v[108:111]
	v_mfma_f32_16x16x32_bf16 v[88:91], v[136:139], v[202:205], v[88:91]
	v_mfma_f32_16x16x32_bf16 v[88:91], v[140:143], v[206:209], v[88:91]
	v_mfma_f32_16x16x32_bf16 v[84:87], v[144:147], v[202:205], v[84:87]
	v_mfma_f32_16x16x32_bf16 v[84:87], v[148:151], v[206:209], v[84:87]
	v_mfma_f32_16x16x32_bf16 v[96:99], v[152:155], v[202:205], v[96:99]
	v_mfma_f32_16x16x32_bf16 v[96:99], v[156:159], v[206:209], v[96:99]
	v_mfma_f32_16x16x32_bf16 v[92:95], v[160:163], v[202:205], v[92:95]
	v_mfma_f32_16x16x32_bf16 v[92:95], v[174:177], v[206:209], v[92:95]
	v_mfma_f32_16x16x32_bf16 v[72:75], v[136:139], v[216:219], v[72:75]
	v_mfma_f32_16x16x32_bf16 v[72:75], v[140:143], v[220:223], v[72:75]
	v_mfma_f32_16x16x32_bf16 v[68:71], v[144:147], v[216:219], v[68:71]
	v_mfma_f32_16x16x32_bf16 v[68:71], v[148:151], v[220:223], v[68:71]
	v_mfma_f32_16x16x32_bf16 v[80:83], v[152:155], v[216:219], v[80:83]
	v_mfma_f32_16x16x32_bf16 v[80:83], v[156:159], v[220:223], v[80:83]
	v_mfma_f32_16x16x32_bf16 v[76:79], v[160:163], v[216:219], v[76:79]
	v_mfma_f32_16x16x32_bf16 v[76:79], v[174:177], v[220:223], v[76:79]
	s_barrier
	s_mov_b32 m0, s46
	ds_read_b128 v[178:181], v200 offset:49152
	ds_read_b128 v[182:185], v200 offset:50176
	ds_read_b128 v[186:189], v200 offset:51200
	ds_read_b128 v[190:193], v200 offset:52224
	ds_read_b128 v[202:205], v200 offset:53248
	ds_read_b128 v[206:209], v200 offset:54272
	ds_read_b128 v[216:219], v200 offset:55296
	ds_read_b128 v[220:223], v200 offset:56320
	s_add_u32 s70, s52, s78
	s_addc_u32 s71, s53, s79
	global_load_lds_dwordx4 v164, s[70:71]
	s_mov_b32 m0, s47
	s_nop 0
	s_add_u32 s70, s52, s84
	s_addc_u32 s71, s53, s85
	global_load_lds_dwordx4 v164, s[70:71]
	s_mov_b32 m0, s48
	s_add_u32 s70, s52, s56
	s_addc_u32 s71, s53, s57
	global_load_lds_dwordx4 v164, s[70:71]
	s_mov_b32 m0, s49
	s_nop 0
	s_add_u32 s70, s52, s62
	s_addc_u32 s71, s53, s63
	global_load_lds_dwordx4 v164, s[70:71]
	s_mov_b32 m0, s38
	s_nop 0
	s_add_u32 s70, s50, s78
	s_addc_u32 s71, s51, s79
	global_load_lds_dwordx4 v166, s[70:71]
	s_mov_b32 m0, s39
	s_nop 0
	s_add_u32 s70, s50, s92
	s_addc_u32 s71, s51, s93
	global_load_lds_dwordx4 v166, s[70:71]
	s_waitcnt vmcnt(8)
	s_waitcnt lgkmcnt(0)
	s_barrier
	v_mfma_f32_16x16x32_bf16 v[56:59], v[136:139], v[178:181], v[56:59]
	v_mfma_f32_16x16x32_bf16 v[56:59], v[140:143], v[182:185], v[56:59]
	v_mfma_f32_16x16x32_bf16 v[52:55], v[144:147], v[178:181], v[52:55]
	v_mfma_f32_16x16x32_bf16 v[52:55], v[148:151], v[182:185], v[52:55]
	v_mfma_f32_16x16x32_bf16 v[64:67], v[152:155], v[178:181], v[64:67]
	v_mfma_f32_16x16x32_bf16 v[64:67], v[156:159], v[182:185], v[64:67]
	v_mfma_f32_16x16x32_bf16 v[60:63], v[160:163], v[178:181], v[60:63]
	v_mfma_f32_16x16x32_bf16 v[60:63], v[174:177], v[182:185], v[60:63]
	v_mfma_f32_16x16x32_bf16 v[40:43], v[136:139], v[186:189], v[40:43]
	v_mfma_f32_16x16x32_bf16 v[40:43], v[140:143], v[190:193], v[40:43]
	v_mfma_f32_16x16x32_bf16 v[36:39], v[144:147], v[186:189], v[36:39]
	v_mfma_f32_16x16x32_bf16 v[36:39], v[148:151], v[190:193], v[36:39]
	v_mfma_f32_16x16x32_bf16 v[48:51], v[152:155], v[186:189], v[48:51]
	v_mfma_f32_16x16x32_bf16 v[48:51], v[156:159], v[190:193], v[48:51]
	v_mfma_f32_16x16x32_bf16 v[44:47], v[160:163], v[186:189], v[44:47]
	v_mfma_f32_16x16x32_bf16 v[44:47], v[174:177], v[190:193], v[44:47]
	v_mfma_f32_16x16x32_bf16 v[24:27], v[136:139], v[202:205], v[24:27]
	v_mfma_f32_16x16x32_bf16 v[24:27], v[140:143], v[206:209], v[24:27]
	v_mfma_f32_16x16x32_bf16 v[20:23], v[144:147], v[202:205], v[20:23]
	v_mfma_f32_16x16x32_bf16 v[20:23], v[148:151], v[206:209], v[20:23]
	v_mfma_f32_16x16x32_bf16 v[32:35], v[152:155], v[202:205], v[32:35]
	v_mfma_f32_16x16x32_bf16 v[32:35], v[156:159], v[206:209], v[32:35]
	v_mfma_f32_16x16x32_bf16 v[28:31], v[160:163], v[202:205], v[28:31]
	v_mfma_f32_16x16x32_bf16 v[28:31], v[174:177], v[206:209], v[28:31]
	v_mfma_f32_16x16x32_bf16 v[8:11], v[136:139], v[216:219], v[8:11]
	v_mfma_f32_16x16x32_bf16 v[8:11], v[140:143], v[220:223], v[8:11]
	v_mfma_f32_16x16x32_bf16 v[4:7], v[144:147], v[216:219], v[4:7]
	v_mfma_f32_16x16x32_bf16 v[4:7], v[148:151], v[220:223], v[4:7]
	v_mfma_f32_16x16x32_bf16 v[16:19], v[152:155], v[216:219], v[16:19]
	v_mfma_f32_16x16x32_bf16 v[16:19], v[156:159], v[220:223], v[16:19]
	v_mfma_f32_16x16x32_bf16 v[12:15], v[160:163], v[216:219], v[12:15]
	v_mfma_f32_16x16x32_bf16 v[12:15], v[174:177], v[220:223], v[12:15]
	s_barrier
	s_add_i32 s14, s14, 2
	s_add_u32 s10, s10, 0x100
	s_addc_u32 s11, s11, 0
	s_add_u32 s12, s12, 0x100
	s_addc_u32 s13, s13, 0
	s_cmp_gt_u32 s14, 29
	s_cbranch_scc0 .LBB0_324
	s_and_b64 vcc, exec, s[18:19]
	s_cbranch_vccz .LBB0_327
	s_barrier

.LBB0_594:
	ds_read_b128 v[136:139], v116
	ds_read_b128 v[140:143], v116 offset:1024
	ds_read_b128 v[144:147], v116 offset:2048
	ds_read_b128 v[148:151], v116 offset:3072
	ds_read_b128 v[152:155], v117
	ds_read_b128 v[156:159], v117 offset:1024
	ds_read_b128 v[160:163], v117 offset:2048
	ds_read_b128 v[164:167], v117 offset:3072
	s_add_u32 s43, s20, 0xfff7c080
	s_addc_u32 s44, s21, -1
	s_cmp_eq_u32 s15, 28
	s_cselect_b32 s45, s17, s44
	s_cselect_b32 s44, s16, s43
	s_cselect_b32 s47, s4, s9
	s_cselect_b32 s46, s5, s8
	s_mov_b32 m0, s33
	ds_read_b128 v[168:171], v221
	ds_read_b128 v[172:175], v221 offset:1024
	ds_read_b128 v[176:179], v221 offset:2048
	ds_read_b128 v[180:183], v221 offset:3072
	ds_read_b128 v[184:187], v221 offset:4096
	ds_read_b128 v[188:191], v221 offset:5120
	ds_read_b128 v[202:205], v221 offset:6144
	ds_read_b128 v[206:209], v221 offset:7168
	global_load_lds_dwordx4 v200, s[20:21]
	s_mov_b32 m0, s34
	s_nop 0
	s_add_u32 s70, s20, s96
	s_addc_u32 s71, s21, s97
	global_load_lds_dwordx4 v200, s[70:71]
	s_waitcnt vmcnt(8)
	s_waitcnt lgkmcnt(0)
	s_barrier
	v_mfma_f32_16x16x32_bf16 v[130:133], v[136:139], v[168:171], v[130:133]
	v_mfma_f32_16x16x32_bf16 v[130:133], v[140:143], v[172:175], v[130:133]
	v_mfma_f32_16x16x32_bf16 v[126:129], v[144:147], v[168:171], v[126:129]
	v_mfma_f32_16x16x32_bf16 v[126:129], v[148:151], v[172:175], v[126:129]
	v_mfma_f32_16x16x32_bf16 v[122:125], v[152:155], v[168:171], v[122:125]
	v_mfma_f32_16x16x32_bf16 v[122:125], v[156:159], v[172:175], v[122:125]
	v_mfma_f32_16x16x32_bf16 v[118:121], v[160:163], v[168:171], v[118:121]
	v_mfma_f32_16x16x32_bf16 v[118:121], v[164:167], v[172:175], v[118:121]
	v_mfma_f32_16x16x32_bf16 v[112:115], v[136:139], v[176:179], v[112:115]
	v_mfma_f32_16x16x32_bf16 v[112:115], v[140:143], v[180:183], v[112:115]
	v_mfma_f32_16x16x32_bf16 v[108:111], v[144:147], v[176:179], v[108:111]
	v_mfma_f32_16x16x32_bf16 v[108:111], v[148:151], v[180:183], v[108:111]
	v_mfma_f32_16x16x32_bf16 v[104:107], v[152:155], v[176:179], v[104:107]
	v_mfma_f32_16x16x32_bf16 v[104:107], v[156:159], v[180:183], v[104:107]
	v_mfma_f32_16x16x32_bf16 v[100:103], v[160:163], v[176:179], v[100:103]
	v_mfma_f32_16x16x32_bf16 v[100:103], v[164:167], v[180:183], v[100:103]
	v_mfma_f32_16x16x32_bf16 v[96:99], v[136:139], v[184:187], v[96:99]
	v_mfma_f32_16x16x32_bf16 v[96:99], v[140:143], v[188:191], v[96:99]
	v_mfma_f32_16x16x32_bf16 v[92:95], v[144:147], v[184:187], v[92:95]
	v_mfma_f32_16x16x32_bf16 v[92:95], v[148:151], v[188:191], v[92:95]
	v_mfma_f32_16x16x32_bf16 v[88:91], v[152:155], v[184:187], v[88:91]
	v_mfma_f32_16x16x32_bf16 v[88:91], v[156:159], v[188:191], v[88:91]
	v_mfma_f32_16x16x32_bf16 v[84:87], v[160:163], v[184:187], v[84:87]
	v_mfma_f32_16x16x32_bf16 v[84:87], v[164:167], v[188:191], v[84:87]
	v_mfma_f32_16x16x32_bf16 v[80:83], v[136:139], v[202:205], v[80:83]
	v_mfma_f32_16x16x32_bf16 v[80:83], v[140:143], v[206:209], v[80:83]
	v_mfma_f32_16x16x32_bf16 v[76:79], v[144:147], v[202:205], v[76:79]
	v_mfma_f32_16x16x32_bf16 v[76:79], v[148:151], v[206:209], v[76:79]
	v_mfma_f32_16x16x32_bf16 v[72:75], v[152:155], v[202:205], v[72:75]
	v_mfma_f32_16x16x32_bf16 v[72:75], v[156:159], v[206:209], v[72:75]
	v_mfma_f32_16x16x32_bf16 v[68:71], v[160:163], v[202:205], v[68:71]
	v_mfma_f32_16x16x32_bf16 v[68:71], v[164:167], v[206:209], v[68:71]
	s_barrier
	s_mov_b32 m0, s35
	ds_read_b128 v[168:171], v221 offset:16384
	ds_read_b128 v[172:175], v221 offset:17408
	ds_read_b128 v[176:179], v221 offset:18432
	ds_read_b128 v[180:183], v221 offset:19456
	ds_read_b128 v[184:187], v221 offset:20480
	ds_read_b128 v[188:191], v221 offset:21504
	ds_read_b128 v[202:205], v221 offset:22528
	ds_read_b128 v[206:209], v221 offset:23552
	global_load_lds_dwordx4 v194, s[46:47]
	s_mov_b32 m0, s36
	s_nop 0
	s_add_u32 s70, s46, s90
	s_addc_u32 s71, s47, s91
	global_load_lds_dwordx4 v194, s[70:71]
	s_mov_b32 m0, s37
	s_nop 0
	s_add_u32 s70, s46, s48
	s_addc_u32 s71, s47, s49
	global_load_lds_dwordx4 v194, s[70:71]
	s_mov_b32 m0, s38
	s_nop 0
	s_add_u32 s70, s46, s52
	s_addc_u32 s71, s47, s53
	global_load_lds_dwordx4 v194, s[70:71]
	s_mov_b32 m0, s23
	s_nop 0
	global_load_lds_dwordx4 v196, s[44:45]
	s_mov_b32 m0, s24
	s_nop 0
	s_add_u32 s70, s44, s96
	s_addc_u32 s71, s45, s97
	global_load_lds_dwordx4 v196, s[70:71]
	s_waitcnt vmcnt(8)
	s_waitcnt lgkmcnt(0)
	s_barrier
	v_mfma_f32_16x16x32_bf16 v[64:67], v[136:139], v[168:171], v[64:67]
	v_mfma_f32_16x16x32_bf16 v[64:67], v[140:143], v[172:175], v[64:67]
	v_mfma_f32_16x16x32_bf16 v[60:63], v[144:147], v[168:171], v[60:63]
	v_mfma_f32_16x16x32_bf16 v[60:63], v[148:151], v[172:175], v[60:63]
	v_mfma_f32_16x16x32_bf16 v[56:59], v[152:155], v[168:171], v[56:59]
	v_mfma_f32_16x16x32_bf16 v[56:59], v[156:159], v[172:175], v[56:59]
	v_mfma_f32_16x16x32_bf16 v[52:55], v[160:163], v[168:171], v[52:55]
	v_mfma_f32_16x16x32_bf16 v[52:55], v[164:167], v[172:175], v[52:55]
	v_mfma_f32_16x16x32_bf16 v[48:51], v[136:139], v[176:179], v[48:51]
	v_mfma_f32_16x16x32_bf16 v[48:51], v[140:143], v[180:183], v[48:51]
	v_mfma_f32_16x16x32_bf16 v[44:47], v[144:147], v[176:179], v[44:47]
	v_mfma_f32_16x16x32_bf16 v[44:47], v[148:151], v[180:183], v[44:47]
	v_mfma_f32_16x16x32_bf16 v[40:43], v[152:155], v[176:179], v[40:43]
	v_mfma_f32_16x16x32_bf16 v[40:43], v[156:159], v[180:183], v[40:43]
	v_mfma_f32_16x16x32_bf16 v[36:39], v[160:163], v[176:179], v[36:39]
	v_mfma_f32_16x16x32_bf16 v[36:39], v[164:167], v[180:183], v[36:39]
	v_mfma_f32_16x16x32_bf16 v[32:35], v[136:139], v[184:187], v[32:35]
	v_mfma_f32_16x16x32_bf16 v[32:35], v[140:143], v[188:191], v[32:35]
	v_mfma_f32_16x16x32_bf16 v[28:31], v[144:147], v[184:187], v[28:31]
	v_mfma_f32_16x16x32_bf16 v[28:31], v[148:151], v[188:191], v[28:31]
	v_mfma_f32_16x16x32_bf16 v[24:27], v[152:155], v[184:187], v[24:27]
	v_mfma_f32_16x16x32_bf16 v[24:27], v[156:159], v[188:191], v[24:27]
	v_mfma_f32_16x16x32_bf16 v[20:23], v[160:163], v[184:187], v[20:23]
	v_mfma_f32_16x16x32_bf16 v[20:23], v[164:167], v[188:191], v[20:23]
	v_mfma_f32_16x16x32_bf16 v[16:19], v[136:139], v[202:205], v[16:19]
	v_mfma_f32_16x16x32_bf16 v[16:19], v[140:143], v[206:209], v[16:19]
	v_mfma_f32_16x16x32_bf16 v[12:15], v[144:147], v[202:205], v[12:15]
	v_mfma_f32_16x16x32_bf16 v[12:15], v[148:151], v[206:209], v[12:15]
	v_mfma_f32_16x16x32_bf16 v[8:11], v[152:155], v[202:205], v[8:11]
	v_mfma_f32_16x16x32_bf16 v[8:11], v[156:159], v[206:209], v[8:11]
	v_mfma_f32_16x16x32_bf16 v[4:7], v[160:163], v[202:205], v[4:7]
	v_mfma_f32_16x16x32_bf16 v[4:7], v[164:167], v[206:209], v[4:7]
	s_barrier
; #define PG8_MMA(ai, bj, At, Bt) do { __builtin_amdgcn_s_setprio(1); _Pragma("unroll") for (int m = 0; m < 4; ++m) _Pragma("unroll") for (int n = 0; n < 2; ++n) _Pragma("unroll") for (int k = 0; k < 2; ++k) \
;         acc[ai][bj][m][n] = __builtin_amdgcn_mfma_f32_16x16x32_bf16(Bt[n][k], At[m][k], acc[ai][bj][m][n], 0, 0, 0); __builtin_amdgcn_s_setprio(0); } while (0)
; #define PG8_WAIT_V(n) asm volatile("s_waitcnt vmcnt(" #n ")" ::: "memory")
; #define PG8_TRIP_HEAD(T) const int t = (T); const bool last = (t == nt - 2); \
;             const char* a1 = cA + (size_t)(t + 1) * kstep; \
;             const char* a2 = last ? nA : cA + (size_t)(t + 2) * kstep; const char* b2 = last ? nB : cB + (size_t)(t + 2) * kstep; \
;             const char* a3 = a2 + kstep; const char* b3 = b2 + kstep; \
;             if (last && has_next) S.a_ready(nxt);
; template <class Epi, class Sched, bool ALIGN_EPI = false, bool SP2 = false>
; __device__ __forceinline__ void gemm_phase(PG8_LAS unsigned char* lds, const Gemm g, const Sched& S, const Epi& E) {
;     ...
;         if constexpr (SP2) {
;             { PG8_TRIP_HEAD(0) PG8_TRIP_SP2(asm volatile("s_waitcnt vmcnt(%0)" :: "n"(8 + Epi::NST) : "memory"), PG8_MMAZ) }
;             for (int tt = 2; tt < nt; tt += 2) { PG8_TRIP_HEAD(tt) PG8_TRIP_SP2(PG8_WAIT_V(8), PG8_MMA) }
	ds_read_b128 v[136:139], v134
	ds_read_b128 v[140:143], v134 offset:1024
	ds_read_b128 v[144:147], v134 offset:2048
	ds_read_b128 v[148:151], v134 offset:3072
	ds_read_b128 v[152:155], v135
	ds_read_b128 v[156:159], v135 offset:1024
	ds_read_b128 v[160:163], v135 offset:2048
	ds_read_b128 v[164:167], v135 offset:3072
	s_mov_b32 m0, s25
	ds_read_b128 v[168:171], v221 offset:32768
	ds_read_b128 v[172:175], v221 offset:33792
	ds_read_b128 v[176:179], v221 offset:34816
	ds_read_b128 v[180:183], v221 offset:35840
	ds_read_b128 v[184:187], v221 offset:36864
	ds_read_b128 v[188:191], v221 offset:37888
	ds_read_b128 v[202:205], v221 offset:38912
	ds_read_b128 v[206:209], v221 offset:39936
	s_add_u32 s70, s44, s82
	s_addc_u32 s71, s45, s83
	global_load_lds_dwordx4 v196, s[70:71]
	s_mov_b32 m0, s26
	s_nop 0
	s_add_u32 s70, s44, s56
	s_addc_u32 s71, s45, s57
	global_load_lds_dwordx4 v196, s[70:71]
	s_waitcnt vmcnt(8)
	s_waitcnt lgkmcnt(0)
	s_barrier
	v_mfma_f32_16x16x32_bf16 v[130:133], v[136:139], v[168:171], v[130:133]
	v_mfma_f32_16x16x32_bf16 v[130:133], v[140:143], v[172:175], v[130:133]
	v_mfma_f32_16x16x32_bf16 v[126:129], v[144:147], v[168:171], v[126:129]
	v_mfma_f32_16x16x32_bf16 v[126:129], v[148:151], v[172:175], v[126:129]
	v_mfma_f32_16x16x32_bf16 v[122:125], v[152:155], v[168:171], v[122:125]
	v_mfma_f32_16x16x32_bf16 v[122:125], v[156:159], v[172:175], v[122:125]
	v_mfma_f32_16x16x32_bf16 v[118:121], v[160:163], v[168:171], v[118:121]
	v_mfma_f32_16x16x32_bf16 v[118:121], v[164:167], v[172:175], v[118:121]
	v_mfma_f32_16x16x32_bf16 v[112:115], v[136:139], v[176:179], v[112:115]
	v_mfma_f32_16x16x32_bf16 v[112:115], v[140:143], v[180:183], v[112:115]
	v_mfma_f32_16x16x32_bf16 v[108:111], v[144:147], v[176:179], v[108:111]
	v_mfma_f32_16x16x32_bf16 v[108:111], v[148:151], v[180:183], v[108:111]
	v_mfma_f32_16x16x32_bf16 v[104:107], v[152:155], v[176:179], v[104:107]
	v_mfma_f32_16x16x32_bf16 v[104:107], v[156:159], v[180:183], v[104:107]
	v_mfma_f32_16x16x32_bf16 v[100:103], v[160:163], v[176:179], v[100:103]
	v_mfma_f32_16x16x32_bf16 v[100:103], v[164:167], v[180:183], v[100:103]
	v_mfma_f32_16x16x32_bf16 v[96:99], v[136:139], v[184:187], v[96:99]
	v_mfma_f32_16x16x32_bf16 v[96:99], v[140:143], v[188:191], v[96:99]
	v_mfma_f32_16x16x32_bf16 v[92:95], v[144:147], v[184:187], v[92:95]
	v_mfma_f32_16x16x32_bf16 v[92:95], v[148:151], v[188:191], v[92:95]
	v_mfma_f32_16x16x32_bf16 v[88:91], v[152:155], v[184:187], v[88:91]
	v_mfma_f32_16x16x32_bf16 v[88:91], v[156:159], v[188:191], v[88:91]
	v_mfma_f32_16x16x32_bf16 v[84:87], v[160:163], v[184:187], v[84:87]
	v_mfma_f32_16x16x32_bf16 v[84:87], v[164:167], v[188:191], v[84:87]
	v_mfma_f32_16x16x32_bf16 v[80:83], v[136:139], v[202:205], v[80:83]
	v_mfma_f32_16x16x32_bf16 v[80:83], v[140:143], v[206:209], v[80:83]
	v_mfma_f32_16x16x32_bf16 v[76:79], v[144:147], v[202:205], v[76:79]
	v_mfma_f32_16x16x32_bf16 v[76:79], v[148:151], v[206:209], v[76:79]
	v_mfma_f32_16x16x32_bf16 v[72:75], v[152:155], v[202:205], v[72:75]
	v_mfma_f32_16x16x32_bf16 v[72:75], v[156:159], v[206:209], v[72:75]
	v_mfma_f32_16x16x32_bf16 v[68:71], v[160:163], v[202:205], v[68:71]
	v_mfma_f32_16x16x32_bf16 v[68:71], v[164:167], v[206:209], v[68:71]
	s_barrier
	s_mov_b32 m0, s39
	ds_read_b128 v[168:171], v221 offset:49152
	ds_read_b128 v[172:175], v221 offset:50176
	ds_read_b128 v[176:179], v221 offset:51200
	ds_read_b128 v[180:183], v221 offset:52224
	ds_read_b128 v[184:187], v221 offset:53248
	ds_read_b128 v[188:191], v221 offset:54272
	ds_read_b128 v[202:205], v221 offset:55296
	ds_read_b128 v[206:209], v221 offset:56320
	s_add_u32 s70, s46, s78
	s_addc_u32 s71, s47, s79
	global_load_lds_dwordx4 v194, s[70:71]
	s_mov_b32 m0, s40
	s_nop 0
	s_add_u32 s70, s46, s84
	s_addc_u32 s71, s47, s85
	global_load_lds_dwordx4 v194, s[70:71]
	s_mov_b32 m0, s41
	s_add_u32 s70, s46, s50
	s_addc_u32 s71, s47, s51
	global_load_lds_dwordx4 v194, s[70:71]
	s_mov_b32 m0, s42
	s_nop 0
	s_add_u32 s70, s46, s54
	s_addc_u32 s71, s47, s55
	global_load_lds_dwordx4 v194, s[70:71]
	s_mov_b32 m0, s27
	s_nop 0
	s_add_u32 s70, s44, s78
	s_addc_u32 s71, s45, s79
	global_load_lds_dwordx4 v196, s[70:71]
	s_mov_b32 m0, s28
	s_nop 0
	s_add_u32 s70, s44, s92
	s_addc_u32 s71, s45, s93
	global_load_lds_dwordx4 v196, s[70:71]
	s_waitcnt vmcnt(8)
	s_waitcnt lgkmcnt(0)
	s_barrier
	v_mfma_f32_16x16x32_bf16 v[64:67], v[136:139], v[168:171], v[64:67]
	v_mfma_f32_16x16x32_bf16 v[64:67], v[140:143], v[172:175], v[64:67]
	v_mfma_f32_16x16x32_bf16 v[60:63], v[144:147], v[168:171], v[60:63]
	v_mfma_f32_16x16x32_bf16 v[60:63], v[148:151], v[172:175], v[60:63]
	v_mfma_f32_16x16x32_bf16 v[56:59], v[152:155], v[168:171], v[56:59]
	v_mfma_f32_16x16x32_bf16 v[56:59], v[156:159], v[172:175], v[56:59]
	v_mfma_f32_16x16x32_bf16 v[52:55], v[160:163], v[168:171], v[52:55]
	v_mfma_f32_16x16x32_bf16 v[52:55], v[164:167], v[172:175], v[52:55]
	v_mfma_f32_16x16x32_bf16 v[48:51], v[136:139], v[176:179], v[48:51]
	v_mfma_f32_16x16x32_bf16 v[48:51], v[140:143], v[180:183], v[48:51]
	v_mfma_f32_16x16x32_bf16 v[44:47], v[144:147], v[176:179], v[44:47]
	v_mfma_f32_16x16x32_bf16 v[44:47], v[148:151], v[180:183], v[44:47]
	v_mfma_f32_16x16x32_bf16 v[40:43], v[152:155], v[176:179], v[40:43]
	v_mfma_f32_16x16x32_bf16 v[40:43], v[156:159], v[180:183], v[40:43]
	v_mfma_f32_16x16x32_bf16 v[36:39], v[160:163], v[176:179], v[36:39]
	v_mfma_f32_16x16x32_bf16 v[36:39], v[164:167], v[180:183], v[36:39]
	v_mfma_f32_16x16x32_bf16 v[32:35], v[136:139], v[184:187], v[32:35]
	v_mfma_f32_16x16x32_bf16 v[32:35], v[140:143], v[188:191], v[32:35]
	v_mfma_f32_16x16x32_bf16 v[28:31], v[144:147], v[184:187], v[28:31]
	v_mfma_f32_16x16x32_bf16 v[28:31], v[148:151], v[188:191], v[28:31]
	v_mfma_f32_16x16x32_bf16 v[24:27], v[152:155], v[184:187], v[24:27]
	v_mfma_f32_16x16x32_bf16 v[24:27], v[156:159], v[188:191], v[24:27]
	v_mfma_f32_16x16x32_bf16 v[20:23], v[160:163], v[184:187], v[20:23]
	v_mfma_f32_16x16x32_bf16 v[20:23], v[164:167], v[188:191], v[20:23]
	v_mfma_f32_16x16x32_bf16 v[16:19], v[136:139], v[202:205], v[16:19]
	v_mfma_f32_16x16x32_bf16 v[16:19], v[140:143], v[206:209], v[16:19]
	v_mfma_f32_16x16x32_bf16 v[12:15], v[144:147], v[202:205], v[12:15]
	v_mfma_f32_16x16x32_bf16 v[12:15], v[148:151], v[206:209], v[12:15]
	v_mfma_f32_16x16x32_bf16 v[8:11], v[152:155], v[202:205], v[8:11]
	v_mfma_f32_16x16x32_bf16 v[8:11], v[156:159], v[206:209], v[8:11]
	v_mfma_f32_16x16x32_bf16 v[4:7], v[160:163], v[202:205], v[4:7]
	v_mfma_f32_16x16x32_bf16 v[4:7], v[164:167], v[206:209], v[4:7]
	s_barrier
	s_add_i32 s15, s15, 2
	s_add_u32 s20, s20, 0x100
	s_addc_u32 s21, s21, 0
	s_add_u32 s8, s8, 0x100
	s_addc_u32 s9, s9, 0
	s_cmp_gt_u32 s15, 29
	s_cbranch_scc0 .LBB0_594
	s_and_b64 vcc, exec, s[12:13]
	s_cbranch_vccz .LBB0_597
	s_barrier

.LBB0_700:
	ds_read_b128 v[120:123], v116
	ds_read_b128 v[132:135], v116 offset:1024
	ds_read_b128 v[144:147], v116 offset:2048
	ds_read_b128 v[148:151], v116 offset:3072
	ds_read_b128 v[152:155], v117
	ds_read_b128 v[156:159], v117 offset:1024
	ds_read_b128 v[166:169], v117 offset:2048
	ds_read_b128 v[170:173], v117 offset:3072
	s_add_u32 s27, s10, 0xfff7c080
	s_addc_u32 s47, s11, -1
	s_cmp_eq_u32 s26, 28
	s_cselect_b32 s49, s21, s47
	s_cselect_b32 s48, s20, s27
	s_cselect_b32 s51, s3, s25
	s_cselect_b32 s50, s4, s24
	s_mov_b32 m0, s5
	ds_read_b128 v[180:183], v178
	ds_read_b128 v[184:187], v178 offset:1024
	ds_read_b128 v[188:191], v178 offset:2048
	ds_read_b128 v[192:195], v178 offset:3072
	ds_read_b128 v[196:199], v178 offset:4096
	ds_read_b128 v[200:203], v178 offset:5120
	ds_read_b128 v[204:207], v178 offset:6144
	ds_read_b128 v[214:217], v178 offset:7168
	global_load_lds_dwordx4 v164, s[10:11]
	s_mov_b32 m0, s19
	s_nop 0
	s_add_u32 s70, s10, s96
	s_addc_u32 s71, s11, s97
	global_load_lds_dwordx4 v164, s[70:71]
	s_waitcnt vmcnt(8)
	s_waitcnt lgkmcnt(0)
	s_barrier
	v_mfma_f32_16x16x32_bf16 v[140:143], v[120:123], v[180:183], v[140:143]
	v_mfma_f32_16x16x32_bf16 v[140:143], v[132:135], v[184:187], v[140:143]
	v_mfma_f32_16x16x32_bf16 v[136:139], v[144:147], v[180:183], v[136:139]
	v_mfma_f32_16x16x32_bf16 v[136:139], v[148:151], v[184:187], v[136:139]
	v_mfma_f32_16x16x32_bf16 v[128:131], v[152:155], v[180:183], v[128:131]
	v_mfma_f32_16x16x32_bf16 v[128:131], v[156:159], v[184:187], v[128:131]
	v_mfma_f32_16x16x32_bf16 v[124:127], v[166:169], v[180:183], v[124:127]
	v_mfma_f32_16x16x32_bf16 v[124:127], v[170:173], v[184:187], v[124:127]
	v_mfma_f32_16x16x32_bf16 v[112:115], v[120:123], v[188:191], v[112:115]
	v_mfma_f32_16x16x32_bf16 v[112:115], v[132:135], v[192:195], v[112:115]
	v_mfma_f32_16x16x32_bf16 v[108:111], v[144:147], v[188:191], v[108:111]
	v_mfma_f32_16x16x32_bf16 v[108:111], v[148:151], v[192:195], v[108:111]
	v_mfma_f32_16x16x32_bf16 v[104:107], v[152:155], v[188:191], v[104:107]
	v_mfma_f32_16x16x32_bf16 v[104:107], v[156:159], v[192:195], v[104:107]
	v_mfma_f32_16x16x32_bf16 v[100:103], v[166:169], v[188:191], v[100:103]
	v_mfma_f32_16x16x32_bf16 v[100:103], v[170:173], v[192:195], v[100:103]
	v_mfma_f32_16x16x32_bf16 v[96:99], v[120:123], v[196:199], v[96:99]
	v_mfma_f32_16x16x32_bf16 v[96:99], v[132:135], v[200:203], v[96:99]
	v_mfma_f32_16x16x32_bf16 v[92:95], v[144:147], v[196:199], v[92:95]
	v_mfma_f32_16x16x32_bf16 v[92:95], v[148:151], v[200:203], v[92:95]
	v_mfma_f32_16x16x32_bf16 v[88:91], v[152:155], v[196:199], v[88:91]
	v_mfma_f32_16x16x32_bf16 v[88:91], v[156:159], v[200:203], v[88:91]
	v_mfma_f32_16x16x32_bf16 v[84:87], v[166:169], v[196:199], v[84:87]
	v_mfma_f32_16x16x32_bf16 v[84:87], v[170:173], v[200:203], v[84:87]
	v_mfma_f32_16x16x32_bf16 v[80:83], v[120:123], v[204:207], v[80:83]
	v_mfma_f32_16x16x32_bf16 v[80:83], v[132:135], v[214:217], v[80:83]
	v_mfma_f32_16x16x32_bf16 v[76:79], v[144:147], v[204:207], v[76:79]
	v_mfma_f32_16x16x32_bf16 v[76:79], v[148:151], v[214:217], v[76:79]
	v_mfma_f32_16x16x32_bf16 v[72:75], v[152:155], v[204:207], v[72:75]
	v_mfma_f32_16x16x32_bf16 v[72:75], v[156:159], v[214:217], v[72:75]
	v_mfma_f32_16x16x32_bf16 v[68:71], v[166:169], v[204:207], v[68:71]
	v_mfma_f32_16x16x32_bf16 v[68:71], v[170:173], v[214:217], v[68:71]
	s_barrier
	s_mov_b32 m0, s33
	ds_read_b128 v[180:183], v178 offset:16384
	ds_read_b128 v[184:187], v178 offset:17408
	ds_read_b128 v[188:191], v178 offset:18432
	ds_read_b128 v[192:195], v178 offset:19456
	ds_read_b128 v[196:199], v178 offset:20480
	ds_read_b128 v[200:203], v178 offset:21504
	ds_read_b128 v[204:207], v178 offset:22528
	ds_read_b128 v[214:217], v178 offset:23552
	global_load_lds_dwordx4 v160, s[50:51]
	s_mov_b32 m0, s40
	s_nop 0
	s_add_u32 s70, s50, s90
	s_addc_u32 s71, s51, s91
	global_load_lds_dwordx4 v160, s[70:71]
	s_mov_b32 m0, s41
	s_nop 0
	s_add_u32 s70, s50, s52
	s_addc_u32 s71, s51, s53
	global_load_lds_dwordx4 v160, s[70:71]
	s_mov_b32 m0, s42
	s_nop 0
	s_add_u32 s70, s50, s56
	s_addc_u32 s71, s51, s57
	global_load_lds_dwordx4 v160, s[70:71]
	s_mov_b32 m0, s29
	s_nop 0
	global_load_lds_dwordx4 v162, s[48:49]
	s_mov_b32 m0, s30
	s_nop 0
	s_add_u32 s70, s48, s96
	s_addc_u32 s71, s49, s97
	global_load_lds_dwordx4 v162, s[70:71]
	s_waitcnt vmcnt(8)
	s_waitcnt lgkmcnt(0)
	s_barrier
	v_mfma_f32_16x16x32_bf16 v[56:59], v[120:123], v[180:183], v[56:59]
	v_mfma_f32_16x16x32_bf16 v[56:59], v[132:135], v[184:187], v[56:59]
	v_mfma_f32_16x16x32_bf16 v[52:55], v[144:147], v[180:183], v[52:55]
	v_mfma_f32_16x16x32_bf16 v[52:55], v[148:151], v[184:187], v[52:55]
	v_mfma_f32_16x16x32_bf16 v[64:67], v[152:155], v[180:183], v[64:67]
	v_mfma_f32_16x16x32_bf16 v[64:67], v[156:159], v[184:187], v[64:67]
	v_mfma_f32_16x16x32_bf16 v[60:63], v[166:169], v[180:183], v[60:63]
	v_mfma_f32_16x16x32_bf16 v[60:63], v[170:173], v[184:187], v[60:63]
	v_mfma_f32_16x16x32_bf16 v[48:51], v[120:123], v[188:191], v[48:51]
	v_mfma_f32_16x16x32_bf16 v[48:51], v[132:135], v[192:195], v[48:51]
	v_mfma_f32_16x16x32_bf16 v[44:47], v[144:147], v[188:191], v[44:47]
	v_mfma_f32_16x16x32_bf16 v[44:47], v[148:151], v[192:195], v[44:47]
	v_mfma_f32_16x16x32_bf16 v[40:43], v[152:155], v[188:191], v[40:43]
	v_mfma_f32_16x16x32_bf16 v[40:43], v[156:159], v[192:195], v[40:43]
	v_mfma_f32_16x16x32_bf16 v[36:39], v[166:169], v[188:191], v[36:39]
	v_mfma_f32_16x16x32_bf16 v[36:39], v[170:173], v[192:195], v[36:39]
	v_mfma_f32_16x16x32_bf16 v[32:35], v[120:123], v[196:199], v[32:35]
	v_mfma_f32_16x16x32_bf16 v[32:35], v[132:135], v[200:203], v[32:35]
	v_mfma_f32_16x16x32_bf16 v[28:31], v[144:147], v[196:199], v[28:31]
	v_mfma_f32_16x16x32_bf16 v[28:31], v[148:151], v[200:203], v[28:31]
	v_mfma_f32_16x16x32_bf16 v[24:27], v[152:155], v[196:199], v[24:27]
	v_mfma_f32_16x16x32_bf16 v[24:27], v[156:159], v[200:203], v[24:27]
	v_mfma_f32_16x16x32_bf16 v[20:23], v[166:169], v[196:199], v[20:23]
	v_mfma_f32_16x16x32_bf16 v[20:23], v[170:173], v[200:203], v[20:23]
	v_mfma_f32_16x16x32_bf16 v[16:19], v[120:123], v[204:207], v[16:19]
	v_mfma_f32_16x16x32_bf16 v[16:19], v[132:135], v[214:217], v[16:19]
	v_mfma_f32_16x16x32_bf16 v[12:15], v[144:147], v[204:207], v[12:15]
	v_mfma_f32_16x16x32_bf16 v[12:15], v[148:151], v[214:217], v[12:15]
	v_mfma_f32_16x16x32_bf16 v[8:11], v[152:155], v[204:207], v[8:11]
	v_mfma_f32_16x16x32_bf16 v[8:11], v[156:159], v[214:217], v[8:11]
	v_mfma_f32_16x16x32_bf16 v[4:7], v[166:169], v[204:207], v[4:7]
	v_mfma_f32_16x16x32_bf16 v[4:7], v[170:173], v[214:217], v[4:7]
	s_barrier
; #define PG8_MMA(ai, bj, At, Bt) do { __builtin_amdgcn_s_setprio(1); _Pragma("unroll") for (int m = 0; m < 4; ++m) _Pragma("unroll") for (int n = 0; n < 2; ++n) _Pragma("unroll") for (int k = 0; k < 2; ++k) \
;         acc[ai][bj][m][n] = __builtin_amdgcn_mfma_f32_16x16x32_bf16(Bt[n][k], At[m][k], acc[ai][bj][m][n], 0, 0, 0); __builtin_amdgcn_s_setprio(0); } while (0)
; #define PG8_WAIT_V(n) asm volatile("s_waitcnt vmcnt(" #n ")" ::: "memory")
; #define PG8_TRIP_HEAD(T) const int t = (T); const bool last = (t == nt - 2); \
;             const char* a1 = cA + (size_t)(t + 1) * kstep; \
;             const char* a2 = last ? nA : cA + (size_t)(t + 2) * kstep; const char* b2 = last ? nB : cB + (size_t)(t + 2) * kstep; \
;             const char* a3 = a2 + kstep; const char* b3 = b2 + kstep; \
;             if (last && has_next) S.a_ready(nxt);
; template <class Epi, class Sched, bool ALIGN_EPI = false, bool SP2 = false>
; __device__ __forceinline__ void gemm_phase(PG8_LAS unsigned char* lds, const Gemm g, const Sched& S, const Epi& E) {
;     ...
;         if constexpr (SP2) {
;             { PG8_TRIP_HEAD(0) PG8_TRIP_SP2(asm volatile("s_waitcnt vmcnt(%0)" :: "n"(8 + Epi::NST) : "memory"), PG8_MMAZ) }
;             for (int tt = 2; tt < nt; tt += 2) { PG8_TRIP_HEAD(tt) PG8_TRIP_SP2(PG8_WAIT_V(8), PG8_MMA) }
	ds_read_b128 v[120:123], v118
	ds_read_b128 v[132:135], v118 offset:1024
	ds_read_b128 v[144:147], v118 offset:2048
	ds_read_b128 v[148:151], v118 offset:3072
	ds_read_b128 v[152:155], v119
	ds_read_b128 v[156:159], v119 offset:1024
	ds_read_b128 v[166:169], v119 offset:2048
	ds_read_b128 v[170:173], v119 offset:3072
	s_mov_b32 m0, s31
	ds_read_b128 v[180:183], v178 offset:32768
	ds_read_b128 v[184:187], v178 offset:33792
	ds_read_b128 v[188:191], v178 offset:34816
	ds_read_b128 v[192:195], v178 offset:35840
	ds_read_b128 v[196:199], v178 offset:36864
	ds_read_b128 v[200:203], v178 offset:37888
	ds_read_b128 v[204:207], v178 offset:38912
	ds_read_b128 v[214:217], v178 offset:39936
	s_add_u32 s70, s48, s82
	s_addc_u32 s71, s49, s83
	global_load_lds_dwordx4 v162, s[70:71]
	s_mov_b32 m0, s34
	s_nop 0
	s_add_u32 s70, s48, s62
	s_addc_u32 s71, s49, s63
	global_load_lds_dwordx4 v162, s[70:71]
	s_waitcnt vmcnt(8)
	s_waitcnt lgkmcnt(0)
	s_barrier
	v_mfma_f32_16x16x32_bf16 v[140:143], v[120:123], v[180:183], v[140:143]
	v_mfma_f32_16x16x32_bf16 v[140:143], v[132:135], v[184:187], v[140:143]
	v_mfma_f32_16x16x32_bf16 v[136:139], v[144:147], v[180:183], v[136:139]
	v_mfma_f32_16x16x32_bf16 v[136:139], v[148:151], v[184:187], v[136:139]
	v_mfma_f32_16x16x32_bf16 v[128:131], v[152:155], v[180:183], v[128:131]
	v_mfma_f32_16x16x32_bf16 v[128:131], v[156:159], v[184:187], v[128:131]
	v_mfma_f32_16x16x32_bf16 v[124:127], v[166:169], v[180:183], v[124:127]
	v_mfma_f32_16x16x32_bf16 v[124:127], v[170:173], v[184:187], v[124:127]
	v_mfma_f32_16x16x32_bf16 v[112:115], v[120:123], v[188:191], v[112:115]
	v_mfma_f32_16x16x32_bf16 v[112:115], v[132:135], v[192:195], v[112:115]
	v_mfma_f32_16x16x32_bf16 v[108:111], v[144:147], v[188:191], v[108:111]
	v_mfma_f32_16x16x32_bf16 v[108:111], v[148:151], v[192:195], v[108:111]
	v_mfma_f32_16x16x32_bf16 v[104:107], v[152:155], v[188:191], v[104:107]
	v_mfma_f32_16x16x32_bf16 v[104:107], v[156:159], v[192:195], v[104:107]
	v_mfma_f32_16x16x32_bf16 v[100:103], v[166:169], v[188:191], v[100:103]
	v_mfma_f32_16x16x32_bf16 v[100:103], v[170:173], v[192:195], v[100:103]
	v_mfma_f32_16x16x32_bf16 v[96:99], v[120:123], v[196:199], v[96:99]
	v_mfma_f32_16x16x32_bf16 v[96:99], v[132:135], v[200:203], v[96:99]
	v_mfma_f32_16x16x32_bf16 v[92:95], v[144:147], v[196:199], v[92:95]
	v_mfma_f32_16x16x32_bf16 v[92:95], v[148:151], v[200:203], v[92:95]
	v_mfma_f32_16x16x32_bf16 v[88:91], v[152:155], v[196:199], v[88:91]
	v_mfma_f32_16x16x32_bf16 v[88:91], v[156:159], v[200:203], v[88:91]
	v_mfma_f32_16x16x32_bf16 v[84:87], v[166:169], v[196:199], v[84:87]
	v_mfma_f32_16x16x32_bf16 v[84:87], v[170:173], v[200:203], v[84:87]
	v_mfma_f32_16x16x32_bf16 v[80:83], v[120:123], v[204:207], v[80:83]
	v_mfma_f32_16x16x32_bf16 v[80:83], v[132:135], v[214:217], v[80:83]
	v_mfma_f32_16x16x32_bf16 v[76:79], v[144:147], v[204:207], v[76:79]
	v_mfma_f32_16x16x32_bf16 v[76:79], v[148:151], v[214:217], v[76:79]
	v_mfma_f32_16x16x32_bf16 v[72:75], v[152:155], v[204:207], v[72:75]
	v_mfma_f32_16x16x32_bf16 v[72:75], v[156:159], v[214:217], v[72:75]
	v_mfma_f32_16x16x32_bf16 v[68:71], v[166:169], v[204:207], v[68:71]
	v_mfma_f32_16x16x32_bf16 v[68:71], v[170:173], v[214:217], v[68:71]
	s_barrier
	s_mov_b32 m0, s43
	ds_read_b128 v[180:183], v178 offset:49152
	ds_read_b128 v[184:187], v178 offset:50176
	ds_read_b128 v[188:191], v178 offset:51200
	ds_read_b128 v[192:195], v178 offset:52224
	ds_read_b128 v[196:199], v178 offset:53248
	ds_read_b128 v[200:203], v178 offset:54272
	ds_read_b128 v[204:207], v178 offset:55296
	ds_read_b128 v[214:217], v178 offset:56320
	s_add_u32 s70, s50, s78
	s_addc_u32 s71, s51, s79
	global_load_lds_dwordx4 v160, s[70:71]
	s_mov_b32 m0, s44
	s_nop 0
	s_add_u32 s70, s50, s84
	s_addc_u32 s71, s51, s85
	global_load_lds_dwordx4 v160, s[70:71]
	s_mov_b32 m0, s45
	s_add_u32 s70, s50, s54
	s_addc_u32 s71, s51, s55
	global_load_lds_dwordx4 v160, s[70:71]
	s_mov_b32 m0, s46
	s_nop 0
	s_add_u32 s70, s50, s60
	s_addc_u32 s71, s51, s61
	global_load_lds_dwordx4 v160, s[70:71]
	s_mov_b32 m0, s36
	s_nop 0
	s_add_u32 s70, s48, s78
	s_addc_u32 s71, s49, s79
	global_load_lds_dwordx4 v162, s[70:71]
	s_mov_b32 m0, s37
	s_nop 0
	s_add_u32 s70, s48, s92
	s_addc_u32 s71, s49, s93
	global_load_lds_dwordx4 v162, s[70:71]
	s_waitcnt vmcnt(8)
	s_waitcnt lgkmcnt(0)
	s_barrier
	v_mfma_f32_16x16x32_bf16 v[56:59], v[120:123], v[180:183], v[56:59]
	v_mfma_f32_16x16x32_bf16 v[56:59], v[132:135], v[184:187], v[56:59]
	v_mfma_f32_16x16x32_bf16 v[52:55], v[144:147], v[180:183], v[52:55]
	v_mfma_f32_16x16x32_bf16 v[52:55], v[148:151], v[184:187], v[52:55]
	v_mfma_f32_16x16x32_bf16 v[64:67], v[152:155], v[180:183], v[64:67]
	v_mfma_f32_16x16x32_bf16 v[64:67], v[156:159], v[184:187], v[64:67]
	v_mfma_f32_16x16x32_bf16 v[60:63], v[166:169], v[180:183], v[60:63]
	v_mfma_f32_16x16x32_bf16 v[60:63], v[170:173], v[184:187], v[60:63]
	v_mfma_f32_16x16x32_bf16 v[48:51], v[120:123], v[188:191], v[48:51]
	v_mfma_f32_16x16x32_bf16 v[48:51], v[132:135], v[192:195], v[48:51]
	v_mfma_f32_16x16x32_bf16 v[44:47], v[144:147], v[188:191], v[44:47]
	v_mfma_f32_16x16x32_bf16 v[44:47], v[148:151], v[192:195], v[44:47]
	v_mfma_f32_16x16x32_bf16 v[40:43], v[152:155], v[188:191], v[40:43]
	v_mfma_f32_16x16x32_bf16 v[40:43], v[156:159], v[192:195], v[40:43]
	v_mfma_f32_16x16x32_bf16 v[36:39], v[166:169], v[188:191], v[36:39]
	v_mfma_f32_16x16x32_bf16 v[36:39], v[170:173], v[192:195], v[36:39]
	v_mfma_f32_16x16x32_bf16 v[32:35], v[120:123], v[196:199], v[32:35]
	v_mfma_f32_16x16x32_bf16 v[32:35], v[132:135], v[200:203], v[32:35]
	v_mfma_f32_16x16x32_bf16 v[28:31], v[144:147], v[196:199], v[28:31]
	v_mfma_f32_16x16x32_bf16 v[28:31], v[148:151], v[200:203], v[28:31]
	v_mfma_f32_16x16x32_bf16 v[24:27], v[152:155], v[196:199], v[24:27]
	v_mfma_f32_16x16x32_bf16 v[24:27], v[156:159], v[200:203], v[24:27]
	v_mfma_f32_16x16x32_bf16 v[20:23], v[166:169], v[196:199], v[20:23]
	v_mfma_f32_16x16x32_bf16 v[20:23], v[170:173], v[200:203], v[20:23]
	v_mfma_f32_16x16x32_bf16 v[16:19], v[120:123], v[204:207], v[16:19]
	v_mfma_f32_16x16x32_bf16 v[16:19], v[132:135], v[214:217], v[16:19]
	v_mfma_f32_16x16x32_bf16 v[12:15], v[144:147], v[204:207], v[12:15]
	v_mfma_f32_16x16x32_bf16 v[12:15], v[148:151], v[214:217], v[12:15]
	v_mfma_f32_16x16x32_bf16 v[8:11], v[152:155], v[204:207], v[8:11]
	v_mfma_f32_16x16x32_bf16 v[8:11], v[156:159], v[214:217], v[8:11]
	v_mfma_f32_16x16x32_bf16 v[4:7], v[166:169], v[204:207], v[4:7]
	v_mfma_f32_16x16x32_bf16 v[4:7], v[170:173], v[214:217], v[4:7]
	s_barrier
	s_add_i32 s26, s26, 2
	s_add_u32 s10, s10, 0x100
	s_addc_u32 s11, s11, 0
	s_add_u32 s24, s24, 0x100
	s_addc_u32 s25, s25, 0
	s_cmp_gt_u32 s26, 29
	s_cbranch_scc0 .LBB0_700
	s_and_b64 vcc, exec, s[16:17]
	s_cbranch_vccz .LBB0_703
	s_barrier
